# batch ss loads in P8 epilogue; issue all 16 row loads per weight-conversion item (w_up,w_down,w_out) before first wait
# speedup vs baseline: 1.0149x; 1.0149x over previous
; #define GAS __attribute__((address_space(1)))
; #define LAS __attribute__((address_space(3)))
;     ...
;     for (int i = 0; i < 16; ++i) { const int kk = 4 * i + kq;
;         f32x4 v = __builtin_nontemporal_load((const GAS f32x4*)(W + (size_t)(k0 + kk) * ldw + n0 + 4 * c4));
;         v = v * (gk ? gk[k0 + kk] * scale : scale);
;         LAS float* d = scr + kk * 65 + 4 * c4; d[0] = v[0]; d[1] = v[1]; d[2] = v[2]; d[3] = v[3]; }
.LBB0_986:
	s_mov_b32 s100, 0x10000
	s_mov_b32 s101, 0
	global_load_dwordx4 v[64:67], v[12:13], off nt
	v_lshl_add_u64 v[12:13], v[12:13], 0, s[100:101]
	global_load_dwordx4 v[68:71], v[12:13], off nt
	v_lshl_add_u64 v[12:13], v[12:13], 0, s[100:101]
	global_load_dwordx4 v[72:75], v[12:13], off nt
	v_lshl_add_u64 v[12:13], v[12:13], 0, s[100:101]
	global_load_dwordx4 v[76:79], v[12:13], off nt
	v_lshl_add_u64 v[12:13], v[12:13], 0, s[100:101]
	global_load_dwordx4 v[80:83], v[12:13], off nt
	v_lshl_add_u64 v[12:13], v[12:13], 0, s[100:101]
	global_load_dwordx4 v[84:87], v[12:13], off nt
	v_lshl_add_u64 v[12:13], v[12:13], 0, s[100:101]
	global_load_dwordx4 v[88:91], v[12:13], off nt
	v_lshl_add_u64 v[12:13], v[12:13], 0, s[100:101]
	global_load_dwordx4 v[92:95], v[12:13], off nt
	v_lshl_add_u64 v[12:13], v[12:13], 0, s[100:101]
	global_load_dwordx4 v[96:99], v[12:13], off nt
	v_lshl_add_u64 v[12:13], v[12:13], 0, s[100:101]
	global_load_dwordx4 v[100:103], v[12:13], off nt
	v_lshl_add_u64 v[12:13], v[12:13], 0, s[100:101]
	global_load_dwordx4 v[104:107], v[12:13], off nt
	v_lshl_add_u64 v[12:13], v[12:13], 0, s[100:101]
	global_load_dwordx4 v[108:111], v[12:13], off nt
	v_lshl_add_u64 v[12:13], v[12:13], 0, s[100:101]
	global_load_dwordx4 v[112:115], v[12:13], off nt
	v_lshl_add_u64 v[12:13], v[12:13], 0, s[100:101]
	global_load_dwordx4 v[116:119], v[12:13], off nt
	v_lshl_add_u64 v[12:13], v[12:13], 0, s[100:101]
	global_load_dwordx4 v[120:123], v[12:13], off nt
	v_lshl_add_u64 v[12:13], v[12:13], 0, s[100:101]
	global_load_dwordx4 v[124:127], v[12:13], off nt
	s_waitcnt vmcnt(15)
	v_pk_mul_f32 v[64:65], v[64:65], s[94:95] op_sel_hi:[1,0]
	v_pk_mul_f32 v[66:67], v[66:67], s[94:95] op_sel_hi:[1,0]
	ds_write2_b32 v15, v64, v65 offset1:1
	ds_write2_b32 v15, v66, v67 offset0:2 offset1:3
	s_waitcnt vmcnt(14)
	v_pk_mul_f32 v[68:69], v[68:69], s[94:95] op_sel_hi:[1,0]
	v_pk_mul_f32 v[70:71], v[70:71], s[94:95] op_sel_hi:[1,0]
	v_add_u32_e32 v2, 0x410, v15
	ds_write2_b32 v2, v68, v69 offset1:1
	ds_write2_b32 v2, v70, v71 offset0:2 offset1:3
	s_waitcnt vmcnt(13)
	v_pk_mul_f32 v[72:73], v[72:73], s[94:95] op_sel_hi:[1,0]
	v_pk_mul_f32 v[74:75], v[74:75], s[94:95] op_sel_hi:[1,0]
	v_add_u32_e32 v2, 0x820, v15
	ds_write2_b32 v2, v72, v73 offset1:1
	ds_write2_b32 v2, v74, v75 offset0:2 offset1:3
	s_waitcnt vmcnt(12)
	v_pk_mul_f32 v[76:77], v[76:77], s[94:95] op_sel_hi:[1,0]
	v_pk_mul_f32 v[78:79], v[78:79], s[94:95] op_sel_hi:[1,0]
	v_add_u32_e32 v2, 0xc30, v15
	ds_write2_b32 v2, v76, v77 offset1:1
	ds_write2_b32 v2, v78, v79 offset0:2 offset1:3
	s_waitcnt vmcnt(11)
	v_pk_mul_f32 v[80:81], v[80:81], s[94:95] op_sel_hi:[1,0]
	v_pk_mul_f32 v[82:83], v[82:83], s[94:95] op_sel_hi:[1,0]
	v_add_u32_e32 v2, 0x1040, v15
	ds_write2_b32 v2, v80, v81 offset1:1
	ds_write2_b32 v2, v82, v83 offset0:2 offset1:3
	s_waitcnt vmcnt(10)
	v_pk_mul_f32 v[84:85], v[84:85], s[94:95] op_sel_hi:[1,0]
	v_pk_mul_f32 v[86:87], v[86:87], s[94:95] op_sel_hi:[1,0]
	v_add_u32_e32 v2, 0x1450, v15
	ds_write2_b32 v2, v84, v85 offset1:1
	ds_write2_b32 v2, v86, v87 offset0:2 offset1:3
	s_waitcnt vmcnt(9)
	v_pk_mul_f32 v[88:89], v[88:89], s[94:95] op_sel_hi:[1,0]
	v_pk_mul_f32 v[90:91], v[90:91], s[94:95] op_sel_hi:[1,0]
	v_add_u32_e32 v2, 0x1860, v15
	ds_write2_b32 v2, v88, v89 offset1:1
	ds_write2_b32 v2, v90, v91 offset0:2 offset1:3
	s_waitcnt vmcnt(8)
	v_pk_mul_f32 v[92:93], v[92:93], s[94:95] op_sel_hi:[1,0]
	v_pk_mul_f32 v[94:95], v[94:95], s[94:95] op_sel_hi:[1,0]
	v_add_u32_e32 v2, 0x1c70, v15
	ds_write2_b32 v2, v92, v93 offset1:1
	ds_write2_b32 v2, v94, v95 offset0:2 offset1:3
	s_waitcnt vmcnt(7)
	v_pk_mul_f32 v[96:97], v[96:97], s[94:95] op_sel_hi:[1,0]
	v_pk_mul_f32 v[98:99], v[98:99], s[94:95] op_sel_hi:[1,0]
	v_add_u32_e32 v2, 0x2080, v15
	ds_write2_b32 v2, v96, v97 offset1:1
	ds_write2_b32 v2, v98, v99 offset0:2 offset1:3
	s_waitcnt vmcnt(6)
	v_pk_mul_f32 v[100:101], v[100:101], s[94:95] op_sel_hi:[1,0]
	v_pk_mul_f32 v[102:103], v[102:103], s[94:95] op_sel_hi:[1,0]
	v_add_u32_e32 v2, 0x2490, v15
	ds_write2_b32 v2, v100, v101 offset1:1
	ds_write2_b32 v2, v102, v103 offset0:2 offset1:3
	s_waitcnt vmcnt(5)
	v_pk_mul_f32 v[104:105], v[104:105], s[94:95] op_sel_hi:[1,0]
	v_pk_mul_f32 v[106:107], v[106:107], s[94:95] op_sel_hi:[1,0]
	v_add_u32_e32 v2, 0x28a0, v15
	ds_write2_b32 v2, v104, v105 offset1:1
	ds_write2_b32 v2, v106, v107 offset0:2 offset1:3
	s_waitcnt vmcnt(4)
	v_pk_mul_f32 v[108:109], v[108:109], s[94:95] op_sel_hi:[1,0]
	v_pk_mul_f32 v[110:111], v[110:111], s[94:95] op_sel_hi:[1,0]
	v_add_u32_e32 v2, 0x2cb0, v15
	ds_write2_b32 v2, v108, v109 offset1:1
	ds_write2_b32 v2, v110, v111 offset0:2 offset1:3
	s_waitcnt vmcnt(3)
	v_pk_mul_f32 v[112:113], v[112:113], s[94:95] op_sel_hi:[1,0]
	v_pk_mul_f32 v[114:115], v[114:115], s[94:95] op_sel_hi:[1,0]
	v_add_u32_e32 v2, 0x30c0, v15
	ds_write2_b32 v2, v112, v113 offset1:1
	ds_write2_b32 v2, v114, v115 offset0:2 offset1:3
	s_waitcnt vmcnt(2)
	v_pk_mul_f32 v[116:117], v[116:117], s[94:95] op_sel_hi:[1,0]
	v_pk_mul_f32 v[118:119], v[118:119], s[94:95] op_sel_hi:[1,0]
	v_add_u32_e32 v2, 0x34d0, v15
	ds_write2_b32 v2, v116, v117 offset1:1
	ds_write2_b32 v2, v118, v119 offset0:2 offset1:3
	s_waitcnt vmcnt(1)
	v_pk_mul_f32 v[120:121], v[120:121], s[94:95] op_sel_hi:[1,0]
	v_pk_mul_f32 v[122:123], v[122:123], s[94:95] op_sel_hi:[1,0]
	v_add_u32_e32 v2, 0x38e0, v15
	ds_write2_b32 v2, v120, v121 offset1:1
	ds_write2_b32 v2, v122, v123 offset0:2 offset1:3
	s_waitcnt vmcnt(0)
	v_pk_mul_f32 v[124:125], v[124:125], s[94:95] op_sel_hi:[1,0]
	v_pk_mul_f32 v[126:127], v[126:127], s[94:95] op_sel_hi:[1,0]
	v_add_u32_e32 v2, 0x3cf0, v15
	ds_write2_b32 v2, v124, v125 offset1:1
	ds_write2_b32 v2, v126, v127 offset0:2 offset1:3
	v_and_b32_e32 v2, 48, v5
	s_waitcnt lgkmcnt(0)
; #define GAS __attribute__((address_space(1)))
; #define LAS __attribute__((address_space(3)))
; #define LDS_WAIT() asm volatile("s_waitcnt lgkmcnt(0)" ::: "memory")
;     ...
;     LDS_WAIT(); asm volatile("" ::: "memory");
;     const int c = lane & 3;
; #pragma unroll
;     for (int j = 0; j < 4; ++j) { const int n = (lane >> 2) + 16 * j; const LAS float* s = scr + (16 * c) * 65 + n;
;         v4u o; o.x = pg8::pk4_fp8(s[0 * 65], s[1 * 65], s[2 * 65], s[3 * 65]); o.y = pg8::pk4_fp8(s[4 * 65], s[5 * 65], s[6 * 65], s[7 * 65]);
;         o.z = pg8::pk4_fp8(s[8 * 65], s[9 * 65], s[10 * 65], s[11 * 65]); o.w = pg8::pk4_fp8(s[12 * 65], s[13 * 65], s[14 * 65], s[15 * 65]);
;         *(GAS v4u*)(WT + ((size_t)((n0 + n) >> 4) * (K >> 5) + ((k0 + 16 * c) >> 5)) * 512 + ((n0 + n) & 15) * 32 + ((16 * c) & 31)) = o; }
	v_mul_u32_u24_e32 v10, 0x104, v2
	v_and_b32_e32 v8, 16, v5
	v_and_b32_e32 v5, -4, v23
	v_add3_u32 v5, s82, v10, v5
	ds_read2_b32 v[12:13], v5 offset1:16
	v_ashrrev_i32_e32 v15, 2, v23
	v_lshlrev_b32_e32 v6, 5, v15
	v_readlane_b32 s18, v253, 58
	v_and_b32_e32 v6, 0x1e0, v6
	v_mov_b32_e32 v7, v3
	v_readlane_b32 s19, v253, 59
	ds_read2_b32 v[16:17], v5 offset0:65 offset1:81
	ds_read2_b32 v[18:19], v5 offset0:130 offset1:146
	ds_read2_b32 v[20:21], v5 offset0:195 offset1:211
	v_lshl_add_u64 v[6:7], s[18:19], 0, v[6:7]
	v_mov_b32_e32 v9, v3
	v_lshl_add_u64 v[6:7], v[6:7], 0, v[8:9]
	s_waitcnt lgkmcnt(3)
	v_max_f32_e32 v8, v12, v12
	v_med3_f32 v9, v8, s95, v199
	s_waitcnt lgkmcnt(2)
	v_max_f32_e32 v8, v16, v16
	v_med3_f32 v10, v8, s95, v199
	s_waitcnt lgkmcnt(1)
	v_max_f32_e32 v8, v18, v18
	v_add_u32_e32 v22, 0x400, v5
	v_med3_f32 v11, v8, s95, v199
	v_mov_b32_e32 v8, v3
	ds_read2_b32 v[24:25], v22 offset0:4 offset1:20
	v_cvt_pk_fp8_f32 v8, v9, v10
	s_waitcnt lgkmcnt(1)
	v_max_f32_e32 v12, v20, v20
	ds_read2_b32 v[26:27], v22 offset0:69 offset1:85
	ds_read2_b32 v[28:29], v22 offset0:134 offset1:150
	ds_read2_b32 v[30:31], v22 offset0:199 offset1:215
	v_med3_f32 v9, v12, s95, v199
	v_cvt_pk_fp8_f32 v8, v11, v9 op_sel:[0,0,1]
	s_waitcnt lgkmcnt(3)
	v_max_f32_e32 v9, v24, v24
	v_med3_f32 v10, v9, s95, v199
	s_waitcnt lgkmcnt(2)
	v_max_f32_e32 v9, v26, v26
	v_med3_f32 v11, v9, s95, v199
	s_waitcnt lgkmcnt(1)
	v_max_f32_e32 v9, v28, v28
	v_add_u32_e32 v52, 0x800, v5
	v_med3_f32 v12, v9, s95, v199
	v_mov_b32_e32 v9, v3
	ds_read2_b32 v[32:33], v52 offset0:8 offset1:24
	v_cvt_pk_fp8_f32 v9, v10, v11
	s_waitcnt lgkmcnt(1)
	v_max_f32_e32 v16, v30, v30
	ds_read2_b32 v[34:35], v52 offset0:73 offset1:89
	ds_read2_b32 v[36:37], v52 offset0:138 offset1:154
	ds_read2_b32 v[38:39], v52 offset0:203 offset1:219
	v_med3_f32 v10, v16, s95, v199
	v_cvt_pk_fp8_f32 v9, v12, v10 op_sel:[0,0,1]
	s_waitcnt lgkmcnt(3)
	v_max_f32_e32 v10, v32, v32
	v_med3_f32 v11, v10, s95, v199
	s_waitcnt lgkmcnt(2)
	v_max_f32_e32 v10, v34, v34
	v_med3_f32 v12, v10, s95, v199
	s_waitcnt lgkmcnt(1)
	v_max_f32_e32 v10, v36, v36
	v_add_u32_e32 v53, 0xc00, v5
	v_med3_f32 v16, v10, s95, v199
	v_mov_b32_e32 v10, v3
	ds_read2_b32 v[40:41], v53 offset0:12 offset1:28
	v_cvt_pk_fp8_f32 v10, v11, v12
	s_waitcnt lgkmcnt(1)
	v_max_f32_e32 v18, v38, v38
	ds_read2_b32 v[42:43], v53 offset0:77 offset1:93
	ds_read2_b32 v[44:45], v53 offset0:142 offset1:158
	ds_read2_b32 v[46:47], v53 offset0:207 offset1:223
	v_med3_f32 v11, v18, s95, v199
	v_cvt_pk_fp8_f32 v10, v16, v11 op_sel:[0,0,1]
	s_waitcnt lgkmcnt(3)
	v_max_f32_e32 v11, v40, v40
	v_med3_f32 v12, v11, s95, v199
	s_waitcnt lgkmcnt(2)
	v_max_f32_e32 v11, v42, v42
	v_med3_f32 v16, v11, s95, v199
	v_mov_b32_e32 v11, v3
	v_cvt_pk_fp8_f32 v11, v12, v16
	s_waitcnt lgkmcnt(1)
	v_max_f32_e32 v18, v44, v44
	s_waitcnt lgkmcnt(0)
	v_max_f32_e32 v16, v46, v46
	v_add_u32_e32 v15, s4, v15
	s_andn2_b32 s5, s5, 63
	v_med3_f32 v12, v18, s95, v199
	v_med3_f32 v16, v16, s95, v199
	v_ashrrev_i32_e32 v48, 4, v15
	v_or_b32_e32 v2, s5, v2
	v_cvt_pk_fp8_f32 v11, v12, v16 op_sel:[0,0,1]
	v_ashrrev_i32_e32 v49, 31, v48
	v_lshrrev_b32_e32 v2, 5, v2
	v_lshlrev_b64 v[48:49], 18, v[48:49]
	v_lshlrev_b64 v[50:51], 9, v[2:3]
	v_lshl_add_u64 v[48:49], v[6:7], 0, v[48:49]
	v_lshl_add_u64 v[48:49], v[48:49], 0, v[50:51]
	global_store_dwordx4 v[48:49], v[8:11], off
	v_max_f32_e32 v2, v13, v13
	v_med3_f32 v2, v2, s95, v199
	v_max_f32_e32 v8, v17, v17
	v_med3_f32 v9, v8, s95, v199
	v_mov_b32_e32 v8, v3
	v_cvt_pk_fp8_f32 v8, v2, v9
	v_max_f32_e32 v10, v19, v19
	v_max_f32_e32 v9, v21, v21
	v_med3_f32 v2, v10, s95, v199
	v_med3_f32 v9, v9, s95, v199
	v_cvt_pk_fp8_f32 v8, v2, v9 op_sel:[0,0,1]
	v_max_f32_e32 v2, v25, v25
	v_max_f32_e32 v9, v27, v27
	v_med3_f32 v2, v2, s95, v199
	v_med3_f32 v10, v9, s95, v199
	v_mov_b32_e32 v9, v3
	v_cvt_pk_fp8_f32 v9, v2, v10
	v_max_f32_e32 v11, v29, v29
	v_max_f32_e32 v10, v31, v31
	v_med3_f32 v2, v11, s95, v199
	v_med3_f32 v10, v10, s95, v199
	v_cvt_pk_fp8_f32 v9, v2, v10 op_sel:[0,0,1]
	v_max_f32_e32 v2, v33, v33
	v_max_f32_e32 v10, v35, v35
	v_med3_f32 v2, v2, s95, v199
	v_med3_f32 v11, v10, s95, v199
	v_mov_b32_e32 v10, v3
	v_cvt_pk_fp8_f32 v10, v2, v11
	v_max_f32_e32 v12, v37, v37
	v_max_f32_e32 v11, v39, v39
	v_med3_f32 v2, v12, s95, v199
	v_med3_f32 v11, v11, s95, v199
	v_cvt_pk_fp8_f32 v10, v2, v11 op_sel:[0,0,1]
	v_max_f32_e32 v2, v41, v41
	v_max_f32_e32 v11, v43, v43
	v_med3_f32 v2, v2, s95, v199
	v_med3_f32 v12, v11, s95, v199
	v_mov_b32_e32 v11, v3
	v_cvt_pk_fp8_f32 v11, v2, v12
	v_max_f32_e32 v13, v45, v45
	v_max_f32_e32 v12, v47, v47
	v_med3_f32 v2, v13, s95, v199
	v_med3_f32 v12, v12, s95, v199
	v_cvt_pk_fp8_f32 v11, v2, v12 op_sel:[0,0,1]
	v_add_u32_e32 v2, 16, v15
	v_ashrrev_i32_e32 v12, 4, v2
	v_ashrrev_i32_e32 v13, 31, v12
	v_lshlrev_b64 v[12:13], 18, v[12:13]
	v_lshl_add_u64 v[12:13], v[6:7], 0, v[12:13]
	v_lshl_add_u64 v[12:13], v[12:13], 0, v[50:51]
	ds_read2_b32 v[16:17], v5 offset0:32 offset1:48
	global_store_dwordx4 v[12:13], v[8:11], off
	ds_read2_b32 v[12:13], v5 offset0:97 offset1:113
	ds_read2_b32 v[18:19], v5 offset0:162 offset1:178
	ds_read2_b32 v[20:21], v5 offset0:227 offset1:243
	ds_read2_b32 v[24:25], v22 offset0:36 offset1:52
	ds_read2_b32 v[26:27], v22 offset0:101 offset1:117
	ds_read2_b32 v[28:29], v22 offset0:166 offset1:182
	ds_read2_b32 v[30:31], v22 offset0:231 offset1:247
	s_waitcnt lgkmcnt(7)
; #define GAS __attribute__((address_space(1)))
; #define LAS __attribute__((address_space(3)))
; #define LDS_WAIT() asm volatile("s_waitcnt lgkmcnt(0)" ::: "memory")
;     ...
; #pragma unroll
;     for (int j = 0; j < 4; ++j) { const int n = (lane >> 2) + 16 * j; const LAS float* s = scr + (16 * c) * 65 + n;
;         v4u o; o.x = pg8::pk4_fp8(s[0 * 65], s[1 * 65], s[2 * 65], s[3 * 65]); o.y = pg8::pk4_fp8(s[4 * 65], s[5 * 65], s[6 * 65], s[7 * 65]);
;         o.z = pg8::pk4_fp8(s[8 * 65], s[9 * 65], s[10 * 65], s[11 * 65]); o.w = pg8::pk4_fp8(s[12 * 65], s[13 * 65], s[14 * 65], s[15 * 65]);
;         *(GAS v4u*)(WT + ((size_t)((n0 + n) >> 4) * (K >> 5) + ((k0 + 16 * c) >> 5)) * 512 + ((n0 + n) & 15) * 32 + ((16 * c) & 31)) = o; }
;     LDS_WAIT(); asm volatile("" ::: "memory");
	v_max_f32_e32 v2, v16, v16
	s_waitcnt lgkmcnt(6)
	v_max_f32_e32 v5, v12, v12
	s_waitcnt lgkmcnt(5)
	v_max_f32_e32 v8, v18, v18
	v_med3_f32 v2, v2, s95, v199
	v_med3_f32 v5, v5, s95, v199
	v_med3_f32 v9, v8, s95, v199
	v_mov_b32_e32 v8, v3
	v_cvt_pk_fp8_f32 v8, v2, v5
	s_waitcnt lgkmcnt(4)
	v_max_f32_e32 v2, v20, v20
	v_med3_f32 v2, v2, s95, v199
	s_waitcnt lgkmcnt(2)
	v_max_f32_e32 v5, v26, v26
	v_cvt_pk_fp8_f32 v8, v9, v2 op_sel:[0,0,1]
	v_max_f32_e32 v2, v24, v24
	s_waitcnt lgkmcnt(1)
	v_max_f32_e32 v9, v28, v28
	v_med3_f32 v2, v2, s95, v199
	v_med3_f32 v5, v5, s95, v199
	v_med3_f32 v10, v9, s95, v199
	v_mov_b32_e32 v9, v3
	ds_read2_b32 v[32:33], v52 offset0:40 offset1:56
	v_cvt_pk_fp8_f32 v9, v2, v5
	ds_read2_b32 v[34:35], v52 offset0:105 offset1:121
	ds_read2_b32 v[36:37], v52 offset0:170 offset1:186
	ds_read2_b32 v[38:39], v52 offset0:235 offset1:251
	s_waitcnt lgkmcnt(4)
	v_max_f32_e32 v2, v30, v30
	v_med3_f32 v2, v2, s95, v199
	v_cvt_pk_fp8_f32 v9, v10, v2 op_sel:[0,0,1]
	s_waitcnt lgkmcnt(3)
	v_max_f32_e32 v2, v32, v32
	s_waitcnt lgkmcnt(2)
	v_max_f32_e32 v5, v34, v34
	s_waitcnt lgkmcnt(1)
	v_max_f32_e32 v10, v36, v36
	v_med3_f32 v2, v2, s95, v199
	v_med3_f32 v5, v5, s95, v199
	v_med3_f32 v11, v10, s95, v199
	v_mov_b32_e32 v10, v3
	ds_read2_b32 v[40:41], v53 offset0:44 offset1:60
	v_cvt_pk_fp8_f32 v10, v2, v5
	ds_read2_b32 v[42:43], v53 offset0:109 offset1:125
	ds_read2_b32 v[44:45], v53 offset0:174 offset1:190
	ds_read2_b32 v[46:47], v53 offset0:239 offset1:255
	s_waitcnt lgkmcnt(4)
	v_max_f32_e32 v2, v38, v38
	v_med3_f32 v2, v2, s95, v199
	v_cvt_pk_fp8_f32 v10, v11, v2 op_sel:[0,0,1]
	s_waitcnt lgkmcnt(3)
	v_max_f32_e32 v2, v40, v40
	s_waitcnt lgkmcnt(2)
	v_max_f32_e32 v5, v42, v42
	v_med3_f32 v2, v2, s95, v199
	v_med3_f32 v5, v5, s95, v199
	v_mov_b32_e32 v11, v3
	v_cvt_pk_fp8_f32 v11, v2, v5
	s_waitcnt lgkmcnt(1)
	v_max_f32_e32 v12, v44, v44
	s_waitcnt lgkmcnt(0)
	v_max_f32_e32 v5, v46, v46
	v_med3_f32 v2, v12, s95, v199
	v_med3_f32 v5, v5, s95, v199
	v_cvt_pk_fp8_f32 v11, v2, v5 op_sel:[0,0,1]
	v_add_u32_e32 v2, 32, v15
	v_ashrrev_i32_e32 v48, 4, v2
	v_ashrrev_i32_e32 v49, 31, v48
	v_lshlrev_b64 v[48:49], 18, v[48:49]
	v_lshl_add_u64 v[48:49], v[6:7], 0, v[48:49]
	v_lshl_add_u64 v[48:49], v[48:49], 0, v[50:51]
	v_max_f32_e32 v2, v17, v17
	v_max_f32_e32 v5, v13, v13
	global_store_dwordx4 v[48:49], v[8:11], off
	v_med3_f32 v2, v2, s95, v199
	v_med3_f32 v5, v5, s95, v199
	v_mov_b32_e32 v8, v3
	v_cvt_pk_fp8_f32 v8, v2, v5
	v_max_f32_e32 v9, v19, v19
	v_max_f32_e32 v5, v21, v21
	v_med3_f32 v2, v9, s95, v199
	v_med3_f32 v5, v5, s95, v199
	v_cvt_pk_fp8_f32 v8, v2, v5 op_sel:[0,0,1]
	v_max_f32_e32 v2, v25, v25
	v_max_f32_e32 v5, v27, v27
	v_med3_f32 v2, v2, s95, v199
	v_med3_f32 v5, v5, s95, v199
	v_mov_b32_e32 v9, v3
	v_cvt_pk_fp8_f32 v9, v2, v5
	v_max_f32_e32 v10, v29, v29
	v_max_f32_e32 v5, v31, v31
	v_med3_f32 v2, v10, s95, v199
	v_med3_f32 v5, v5, s95, v199
	v_cvt_pk_fp8_f32 v9, v2, v5 op_sel:[0,0,1]
	v_max_f32_e32 v2, v33, v33
	v_max_f32_e32 v5, v35, v35
	v_med3_f32 v2, v2, s95, v199
	v_med3_f32 v5, v5, s95, v199
	v_mov_b32_e32 v10, v3
	v_cvt_pk_fp8_f32 v10, v2, v5
	v_max_f32_e32 v11, v37, v37
	v_max_f32_e32 v5, v39, v39
	v_med3_f32 v2, v11, s95, v199
	v_med3_f32 v5, v5, s95, v199
	v_cvt_pk_fp8_f32 v10, v2, v5 op_sel:[0,0,1]
	v_max_f32_e32 v2, v41, v41
	v_max_f32_e32 v5, v43, v43
	v_med3_f32 v2, v2, s95, v199
	v_med3_f32 v5, v5, s95, v199
	v_mov_b32_e32 v11, v3
	v_cvt_pk_fp8_f32 v11, v2, v5
	v_max_f32_e32 v12, v45, v45
	v_max_f32_e32 v5, v47, v47
	v_med3_f32 v2, v12, s95, v199
	v_med3_f32 v5, v5, s95, v199
	v_cvt_pk_fp8_f32 v11, v2, v5 op_sel:[0,0,1]
	v_add_u32_e32 v2, 48, v15
	v_ashrrev_i32_e32 v12, 4, v2
	v_ashrrev_i32_e32 v13, 31, v12
	v_lshlrev_b64 v[12:13], 18, v[12:13]
	v_lshl_add_u64 v[6:7], v[6:7], 0, v[12:13]
	v_lshl_add_u64 v[6:7], v[6:7], 0, v[50:51]
	global_store_dwordx4 v[6:7], v[8:11], off
	s_waitcnt lgkmcnt(0)
	s_mov_b64 s[4:5], 0

; #define GAS __attribute__((address_space(1)))
;     ...
;     for (int i = 0; i < 16; ++i) { const int kk = 4 * i + kq;
;         f32x4 v = __builtin_nontemporal_load((const GAS f32x4*)(W + (size_t)(k0 + kk) * ldw + n0 + 4 * c4));
;         v = v * (gk ? gk[k0 + kk] * scale : scale);
.LBB0_991:
	s_mov_b32 s100, 0x40000
	s_mov_b32 s101, 0
	s_andn2_b64 vcc, exec, s[68:69]
	s_cbranch_vccnz .Lconv_nogain_up
	v_lshl_add_u64 v[196:197], s[20:21], 0, v[18:19]
	global_load_dword v164, v[196:197], off
	global_load_dword v166, v[196:197], off offset:16
	global_load_dword v168, v[196:197], off offset:32
	global_load_dword v170, v[196:197], off offset:48
	global_load_dword v172, v[196:197], off offset:64
	global_load_dword v174, v[196:197], off offset:80
	global_load_dword v176, v[196:197], off offset:96
	global_load_dword v178, v[196:197], off offset:112
	global_load_dword v180, v[196:197], off offset:128
	global_load_dword v182, v[196:197], off offset:144
	global_load_dword v184, v[196:197], off offset:160
	global_load_dword v186, v[196:197], off offset:176
	global_load_dword v188, v[196:197], off offset:192
	global_load_dword v190, v[196:197], off offset:208
	global_load_dword v192, v[196:197], off offset:224
	global_load_dword v194, v[196:197], off offset:240
	s_branch .Lconv_gdone_up
.Lconv_nogain_up:
	v_mov_b32_e32 v164, 1.0
	v_mov_b32_e32 v166, 1.0
	v_mov_b32_e32 v168, 1.0
	v_mov_b32_e32 v170, 1.0
	v_mov_b32_e32 v172, 1.0
	v_mov_b32_e32 v174, 1.0
	v_mov_b32_e32 v176, 1.0
	v_mov_b32_e32 v178, 1.0
	v_mov_b32_e32 v180, 1.0
	v_mov_b32_e32 v182, 1.0
	v_mov_b32_e32 v184, 1.0
	v_mov_b32_e32 v186, 1.0
	v_mov_b32_e32 v188, 1.0
	v_mov_b32_e32 v190, 1.0
	v_mov_b32_e32 v192, 1.0
	v_mov_b32_e32 v194, 1.0
; #define GAS __attribute__((address_space(1)))
; #define LAS __attribute__((address_space(3)))
;     ...
;     for (int i = 0; i < 16; ++i) { const int kk = 4 * i + kq;
;         f32x4 v = __builtin_nontemporal_load((const GAS f32x4*)(W + (size_t)(k0 + kk) * ldw + n0 + 4 * c4));
;         v = v * (gk ? gk[k0 + kk] * scale : scale);
;         LAS float* d = scr + kk * 65 + 4 * c4; d[0] = v[0]; d[1] = v[1]; d[2] = v[2]; d[3] = v[3]; }
.Lconv_gdone_up:
	global_load_dwordx4 v[64:67], v[16:17], off nt
	v_lshl_add_u64 v[16:17], v[16:17], 0, s[100:101]
	global_load_dwordx4 v[68:71], v[16:17], off nt
	v_lshl_add_u64 v[16:17], v[16:17], 0, s[100:101]
	global_load_dwordx4 v[72:75], v[16:17], off nt
	v_lshl_add_u64 v[16:17], v[16:17], 0, s[100:101]
	global_load_dwordx4 v[76:79], v[16:17], off nt
	v_lshl_add_u64 v[16:17], v[16:17], 0, s[100:101]
	global_load_dwordx4 v[80:83], v[16:17], off nt
	v_lshl_add_u64 v[16:17], v[16:17], 0, s[100:101]
	global_load_dwordx4 v[84:87], v[16:17], off nt
	v_lshl_add_u64 v[16:17], v[16:17], 0, s[100:101]
	global_load_dwordx4 v[88:91], v[16:17], off nt
	v_lshl_add_u64 v[16:17], v[16:17], 0, s[100:101]
	global_load_dwordx4 v[92:95], v[16:17], off nt
	v_lshl_add_u64 v[16:17], v[16:17], 0, s[100:101]
	global_load_dwordx4 v[96:99], v[16:17], off nt
	v_lshl_add_u64 v[16:17], v[16:17], 0, s[100:101]
	global_load_dwordx4 v[100:103], v[16:17], off nt
	v_lshl_add_u64 v[16:17], v[16:17], 0, s[100:101]
	global_load_dwordx4 v[104:107], v[16:17], off nt
	v_lshl_add_u64 v[16:17], v[16:17], 0, s[100:101]
	global_load_dwordx4 v[108:111], v[16:17], off nt
	v_lshl_add_u64 v[16:17], v[16:17], 0, s[100:101]
	global_load_dwordx4 v[112:115], v[16:17], off nt
	v_lshl_add_u64 v[16:17], v[16:17], 0, s[100:101]
	global_load_dwordx4 v[116:119], v[16:17], off nt
	v_lshl_add_u64 v[16:17], v[16:17], 0, s[100:101]
	global_load_dwordx4 v[120:123], v[16:17], off nt
	v_lshl_add_u64 v[16:17], v[16:17], 0, s[100:101]
	global_load_dwordx4 v[124:127], v[16:17], off nt
	s_waitcnt vmcnt(15)
	v_mul_f32_e32 v164, 0x42800000, v164
	v_pk_mul_f32 v[64:65], v[64:65], v[164:165] op_sel_hi:[1,0]
	v_pk_mul_f32 v[66:67], v[66:67], v[164:165] op_sel_hi:[1,0]
	ds_write2_b32 v25, v64, v65 offset1:1
	ds_write2_b32 v25, v66, v67 offset0:2 offset1:3
	s_waitcnt vmcnt(14)
	v_mul_f32_e32 v166, 0x42800000, v166
	v_pk_mul_f32 v[68:69], v[68:69], v[166:167] op_sel_hi:[1,0]
	v_pk_mul_f32 v[70:71], v[70:71], v[166:167] op_sel_hi:[1,0]
	v_add_u32_e32 v2, 0x410, v25
	ds_write2_b32 v2, v68, v69 offset1:1
	ds_write2_b32 v2, v70, v71 offset0:2 offset1:3
	s_waitcnt vmcnt(13)
	v_mul_f32_e32 v168, 0x42800000, v168
	v_pk_mul_f32 v[72:73], v[72:73], v[168:169] op_sel_hi:[1,0]
	v_pk_mul_f32 v[74:75], v[74:75], v[168:169] op_sel_hi:[1,0]
	v_add_u32_e32 v2, 0x820, v25
	ds_write2_b32 v2, v72, v73 offset1:1
	ds_write2_b32 v2, v74, v75 offset0:2 offset1:3
	s_waitcnt vmcnt(12)
	v_mul_f32_e32 v170, 0x42800000, v170
	v_pk_mul_f32 v[76:77], v[76:77], v[170:171] op_sel_hi:[1,0]
	v_pk_mul_f32 v[78:79], v[78:79], v[170:171] op_sel_hi:[1,0]
	v_add_u32_e32 v2, 0xc30, v25
	ds_write2_b32 v2, v76, v77 offset1:1
	ds_write2_b32 v2, v78, v79 offset0:2 offset1:3
	s_waitcnt vmcnt(11)
	v_mul_f32_e32 v172, 0x42800000, v172
	v_pk_mul_f32 v[80:81], v[80:81], v[172:173] op_sel_hi:[1,0]
	v_pk_mul_f32 v[82:83], v[82:83], v[172:173] op_sel_hi:[1,0]
	v_add_u32_e32 v2, 0x1040, v25
	ds_write2_b32 v2, v80, v81 offset1:1
	ds_write2_b32 v2, v82, v83 offset0:2 offset1:3
	s_waitcnt vmcnt(10)
	v_mul_f32_e32 v174, 0x42800000, v174
	v_pk_mul_f32 v[84:85], v[84:85], v[174:175] op_sel_hi:[1,0]
	v_pk_mul_f32 v[86:87], v[86:87], v[174:175] op_sel_hi:[1,0]
	v_add_u32_e32 v2, 0x1450, v25
	ds_write2_b32 v2, v84, v85 offset1:1
	ds_write2_b32 v2, v86, v87 offset0:2 offset1:3
	s_waitcnt vmcnt(9)
	v_mul_f32_e32 v176, 0x42800000, v176
	v_pk_mul_f32 v[88:89], v[88:89], v[176:177] op_sel_hi:[1,0]
	v_pk_mul_f32 v[90:91], v[90:91], v[176:177] op_sel_hi:[1,0]
	v_add_u32_e32 v2, 0x1860, v25
	ds_write2_b32 v2, v88, v89 offset1:1
	ds_write2_b32 v2, v90, v91 offset0:2 offset1:3
	s_waitcnt vmcnt(8)
	v_mul_f32_e32 v178, 0x42800000, v178
	v_pk_mul_f32 v[92:93], v[92:93], v[178:179] op_sel_hi:[1,0]
	v_pk_mul_f32 v[94:95], v[94:95], v[178:179] op_sel_hi:[1,0]
	v_add_u32_e32 v2, 0x1c70, v25
	ds_write2_b32 v2, v92, v93 offset1:1
	ds_write2_b32 v2, v94, v95 offset0:2 offset1:3
	s_waitcnt vmcnt(7)
	v_mul_f32_e32 v180, 0x42800000, v180
	v_pk_mul_f32 v[96:97], v[96:97], v[180:181] op_sel_hi:[1,0]
	v_pk_mul_f32 v[98:99], v[98:99], v[180:181] op_sel_hi:[1,0]
	v_add_u32_e32 v2, 0x2080, v25
	ds_write2_b32 v2, v96, v97 offset1:1
	ds_write2_b32 v2, v98, v99 offset0:2 offset1:3
	s_waitcnt vmcnt(6)
	v_mul_f32_e32 v182, 0x42800000, v182
	v_pk_mul_f32 v[100:101], v[100:101], v[182:183] op_sel_hi:[1,0]
	v_pk_mul_f32 v[102:103], v[102:103], v[182:183] op_sel_hi:[1,0]
	v_add_u32_e32 v2, 0x2490, v25
	ds_write2_b32 v2, v100, v101 offset1:1
	ds_write2_b32 v2, v102, v103 offset0:2 offset1:3
	s_waitcnt vmcnt(5)
	v_mul_f32_e32 v184, 0x42800000, v184
	v_pk_mul_f32 v[104:105], v[104:105], v[184:185] op_sel_hi:[1,0]
	v_pk_mul_f32 v[106:107], v[106:107], v[184:185] op_sel_hi:[1,0]
	v_add_u32_e32 v2, 0x28a0, v25
	ds_write2_b32 v2, v104, v105 offset1:1
	ds_write2_b32 v2, v106, v107 offset0:2 offset1:3
	s_waitcnt vmcnt(4)
	v_mul_f32_e32 v186, 0x42800000, v186
	v_pk_mul_f32 v[108:109], v[108:109], v[186:187] op_sel_hi:[1,0]
	v_pk_mul_f32 v[110:111], v[110:111], v[186:187] op_sel_hi:[1,0]
	v_add_u32_e32 v2, 0x2cb0, v25
	ds_write2_b32 v2, v108, v109 offset1:1
	ds_write2_b32 v2, v110, v111 offset0:2 offset1:3
	s_waitcnt vmcnt(3)
	v_mul_f32_e32 v188, 0x42800000, v188
	v_pk_mul_f32 v[112:113], v[112:113], v[188:189] op_sel_hi:[1,0]
	v_pk_mul_f32 v[114:115], v[114:115], v[188:189] op_sel_hi:[1,0]
	v_add_u32_e32 v2, 0x30c0, v25
	ds_write2_b32 v2, v112, v113 offset1:1
	ds_write2_b32 v2, v114, v115 offset0:2 offset1:3
	s_waitcnt vmcnt(2)
	v_mul_f32_e32 v190, 0x42800000, v190
	v_pk_mul_f32 v[116:117], v[116:117], v[190:191] op_sel_hi:[1,0]
	v_pk_mul_f32 v[118:119], v[118:119], v[190:191] op_sel_hi:[1,0]
	v_add_u32_e32 v2, 0x34d0, v25
	ds_write2_b32 v2, v116, v117 offset1:1
	ds_write2_b32 v2, v118, v119 offset0:2 offset1:3
	s_waitcnt vmcnt(1)
	v_mul_f32_e32 v192, 0x42800000, v192
	v_pk_mul_f32 v[120:121], v[120:121], v[192:193] op_sel_hi:[1,0]
	v_pk_mul_f32 v[122:123], v[122:123], v[192:193] op_sel_hi:[1,0]
	v_add_u32_e32 v2, 0x38e0, v25
	ds_write2_b32 v2, v120, v121 offset1:1
	ds_write2_b32 v2, v122, v123 offset0:2 offset1:3
	s_waitcnt vmcnt(0)
	v_mul_f32_e32 v194, 0x42800000, v194
	v_pk_mul_f32 v[124:125], v[124:125], v[194:195] op_sel_hi:[1,0]
	v_pk_mul_f32 v[126:127], v[126:127], v[194:195] op_sel_hi:[1,0]
	v_add_u32_e32 v2, 0x3cf0, v25
	ds_write2_b32 v2, v124, v125 offset1:1
	ds_write2_b32 v2, v126, v127 offset0:2 offset1:3

; #define GAS __attribute__((address_space(1)))
; #define LAS __attribute__((address_space(3)))
;     ...
;     for (int i = 0; i < 16; ++i) { const int kk = 4 * i + kq;
;         f32x4 v = __builtin_nontemporal_load((const GAS f32x4*)(W + (size_t)(k0 + kk) * ldw + n0 + 4 * c4));
;         v = v * (gk ? gk[k0 + kk] * scale : scale);
;         LAS float* d = scr + kk * 65 + 4 * c4; d[0] = v[0]; d[1] = v[1]; d[2] = v[2]; d[3] = v[3]; }
.LBB0_1026:
	s_mov_b32 s100, 0x10000
	s_mov_b32 s101, 0
	global_load_dwordx4 v[64:67], v[8:9], off nt
	v_lshl_add_u64 v[8:9], v[8:9], 0, s[100:101]
	global_load_dwordx4 v[68:71], v[8:9], off nt
	v_lshl_add_u64 v[8:9], v[8:9], 0, s[100:101]
	global_load_dwordx4 v[72:75], v[8:9], off nt
	v_lshl_add_u64 v[8:9], v[8:9], 0, s[100:101]
	global_load_dwordx4 v[76:79], v[8:9], off nt
	v_lshl_add_u64 v[8:9], v[8:9], 0, s[100:101]
	global_load_dwordx4 v[80:83], v[8:9], off nt
	v_lshl_add_u64 v[8:9], v[8:9], 0, s[100:101]
	global_load_dwordx4 v[84:87], v[8:9], off nt
	v_lshl_add_u64 v[8:9], v[8:9], 0, s[100:101]
	global_load_dwordx4 v[88:91], v[8:9], off nt
	v_lshl_add_u64 v[8:9], v[8:9], 0, s[100:101]
	global_load_dwordx4 v[92:95], v[8:9], off nt
	v_lshl_add_u64 v[8:9], v[8:9], 0, s[100:101]
	global_load_dwordx4 v[96:99], v[8:9], off nt
	v_lshl_add_u64 v[8:9], v[8:9], 0, s[100:101]
	global_load_dwordx4 v[100:103], v[8:9], off nt
	v_lshl_add_u64 v[8:9], v[8:9], 0, s[100:101]
	global_load_dwordx4 v[104:107], v[8:9], off nt
	v_lshl_add_u64 v[8:9], v[8:9], 0, s[100:101]
	global_load_dwordx4 v[108:111], v[8:9], off nt
	v_lshl_add_u64 v[8:9], v[8:9], 0, s[100:101]
	global_load_dwordx4 v[112:115], v[8:9], off nt
	v_lshl_add_u64 v[8:9], v[8:9], 0, s[100:101]
	global_load_dwordx4 v[116:119], v[8:9], off nt
	v_lshl_add_u64 v[8:9], v[8:9], 0, s[100:101]
	global_load_dwordx4 v[120:123], v[8:9], off nt
	v_lshl_add_u64 v[8:9], v[8:9], 0, s[100:101]
	global_load_dwordx4 v[124:127], v[8:9], off nt
	s_waitcnt vmcnt(15)
	v_pk_mul_f32 v[64:65], v[64:65], s[92:93] op_sel_hi:[1,0]
	v_pk_mul_f32 v[66:67], v[66:67], s[92:93] op_sel_hi:[1,0]
	ds_write2_b32 v11, v64, v65 offset1:1
	ds_write2_b32 v11, v66, v67 offset0:2 offset1:3
	s_waitcnt vmcnt(14)
	v_pk_mul_f32 v[68:69], v[68:69], s[92:93] op_sel_hi:[1,0]
	v_pk_mul_f32 v[70:71], v[70:71], s[92:93] op_sel_hi:[1,0]
	v_add_u32_e32 v2, 0x410, v11
	ds_write2_b32 v2, v68, v69 offset1:1
	ds_write2_b32 v2, v70, v71 offset0:2 offset1:3
	s_waitcnt vmcnt(13)
	v_pk_mul_f32 v[72:73], v[72:73], s[92:93] op_sel_hi:[1,0]
	v_pk_mul_f32 v[74:75], v[74:75], s[92:93] op_sel_hi:[1,0]
	v_add_u32_e32 v2, 0x820, v11
	ds_write2_b32 v2, v72, v73 offset1:1
	ds_write2_b32 v2, v74, v75 offset0:2 offset1:3
	s_waitcnt vmcnt(12)
	v_pk_mul_f32 v[76:77], v[76:77], s[92:93] op_sel_hi:[1,0]
	v_pk_mul_f32 v[78:79], v[78:79], s[92:93] op_sel_hi:[1,0]
	v_add_u32_e32 v2, 0xc30, v11
	ds_write2_b32 v2, v76, v77 offset1:1
	ds_write2_b32 v2, v78, v79 offset0:2 offset1:3
	s_waitcnt vmcnt(11)
	v_pk_mul_f32 v[80:81], v[80:81], s[92:93] op_sel_hi:[1,0]
	v_pk_mul_f32 v[82:83], v[82:83], s[92:93] op_sel_hi:[1,0]
	v_add_u32_e32 v2, 0x1040, v11
	ds_write2_b32 v2, v80, v81 offset1:1
	ds_write2_b32 v2, v82, v83 offset0:2 offset1:3
	s_waitcnt vmcnt(10)
	v_pk_mul_f32 v[84:85], v[84:85], s[92:93] op_sel_hi:[1,0]
	v_pk_mul_f32 v[86:87], v[86:87], s[92:93] op_sel_hi:[1,0]
	v_add_u32_e32 v2, 0x1450, v11
	ds_write2_b32 v2, v84, v85 offset1:1
	ds_write2_b32 v2, v86, v87 offset0:2 offset1:3
	s_waitcnt vmcnt(9)
	v_pk_mul_f32 v[88:89], v[88:89], s[92:93] op_sel_hi:[1,0]
	v_pk_mul_f32 v[90:91], v[90:91], s[92:93] op_sel_hi:[1,0]
	v_add_u32_e32 v2, 0x1860, v11
	ds_write2_b32 v2, v88, v89 offset1:1
	ds_write2_b32 v2, v90, v91 offset0:2 offset1:3
	s_waitcnt vmcnt(8)
	v_pk_mul_f32 v[92:93], v[92:93], s[92:93] op_sel_hi:[1,0]
	v_pk_mul_f32 v[94:95], v[94:95], s[92:93] op_sel_hi:[1,0]
	v_add_u32_e32 v2, 0x1c70, v11
	ds_write2_b32 v2, v92, v93 offset1:1
	ds_write2_b32 v2, v94, v95 offset0:2 offset1:3
	s_waitcnt vmcnt(7)
	v_pk_mul_f32 v[96:97], v[96:97], s[92:93] op_sel_hi:[1,0]
	v_pk_mul_f32 v[98:99], v[98:99], s[92:93] op_sel_hi:[1,0]
	v_add_u32_e32 v2, 0x2080, v11
	ds_write2_b32 v2, v96, v97 offset1:1
	ds_write2_b32 v2, v98, v99 offset0:2 offset1:3
	s_waitcnt vmcnt(6)
	v_pk_mul_f32 v[100:101], v[100:101], s[92:93] op_sel_hi:[1,0]
	v_pk_mul_f32 v[102:103], v[102:103], s[92:93] op_sel_hi:[1,0]
	v_add_u32_e32 v2, 0x2490, v11
	ds_write2_b32 v2, v100, v101 offset1:1
	ds_write2_b32 v2, v102, v103 offset0:2 offset1:3
	s_waitcnt vmcnt(5)
	v_pk_mul_f32 v[104:105], v[104:105], s[92:93] op_sel_hi:[1,0]
	v_pk_mul_f32 v[106:107], v[106:107], s[92:93] op_sel_hi:[1,0]
	v_add_u32_e32 v2, 0x28a0, v11
	ds_write2_b32 v2, v104, v105 offset1:1
	ds_write2_b32 v2, v106, v107 offset0:2 offset1:3
	s_waitcnt vmcnt(4)
	v_pk_mul_f32 v[108:109], v[108:109], s[92:93] op_sel_hi:[1,0]
	v_pk_mul_f32 v[110:111], v[110:111], s[92:93] op_sel_hi:[1,0]
	v_add_u32_e32 v2, 0x2cb0, v11
	ds_write2_b32 v2, v108, v109 offset1:1
	ds_write2_b32 v2, v110, v111 offset0:2 offset1:3
	s_waitcnt vmcnt(3)
	v_pk_mul_f32 v[112:113], v[112:113], s[92:93] op_sel_hi:[1,0]
	v_pk_mul_f32 v[114:115], v[114:115], s[92:93] op_sel_hi:[1,0]
	v_add_u32_e32 v2, 0x30c0, v11
	ds_write2_b32 v2, v112, v113 offset1:1
	ds_write2_b32 v2, v114, v115 offset0:2 offset1:3
	s_waitcnt vmcnt(2)
	v_pk_mul_f32 v[116:117], v[116:117], s[92:93] op_sel_hi:[1,0]
	v_pk_mul_f32 v[118:119], v[118:119], s[92:93] op_sel_hi:[1,0]
	v_add_u32_e32 v2, 0x34d0, v11
	ds_write2_b32 v2, v116, v117 offset1:1
	ds_write2_b32 v2, v118, v119 offset0:2 offset1:3
	s_waitcnt vmcnt(1)
	v_pk_mul_f32 v[120:121], v[120:121], s[92:93] op_sel_hi:[1,0]
	v_pk_mul_f32 v[122:123], v[122:123], s[92:93] op_sel_hi:[1,0]
	v_add_u32_e32 v2, 0x38e0, v11
	ds_write2_b32 v2, v120, v121 offset1:1
	ds_write2_b32 v2, v122, v123 offset0:2 offset1:3
	s_waitcnt vmcnt(0)
	v_pk_mul_f32 v[124:125], v[124:125], s[92:93] op_sel_hi:[1,0]
	v_pk_mul_f32 v[126:127], v[126:127], s[92:93] op_sel_hi:[1,0]
	v_add_u32_e32 v2, 0x3cf0, v11
	ds_write2_b32 v2, v124, v125 offset1:1
	ds_write2_b32 v2, v126, v127 offset0:2 offset1:3
	v_and_b32_e32 v2, 48, v10
	v_ashrrev_i32_e32 v44, 2, v23
	v_mul_u32_u24_e32 v6, 0x104, v2
	v_or_b32_e32 v2, s18, v2
	s_waitcnt lgkmcnt(0)
; #define GAS __attribute__((address_space(1)))
; #define LAS __attribute__((address_space(3)))
; #define LDS_WAIT() asm volatile("s_waitcnt lgkmcnt(0)" ::: "memory")
;     ...
;     const int c = lane & 3;
; #pragma unroll
;     for (int j = 0; j < 4; ++j) { const int n = (lane >> 2) + 16 * j; const LAS float* s = scr + (16 * c) * 65 + n;
;         v4u o; o.x = pg8::pk4_fp8(s[0 * 65], s[1 * 65], s[2 * 65], s[3 * 65]); o.y = pg8::pk4_fp8(s[4 * 65], s[5 * 65], s[6 * 65], s[7 * 65]);
;         o.z = pg8::pk4_fp8(s[8 * 65], s[9 * 65], s[10 * 65], s[11 * 65]); o.w = pg8::pk4_fp8(s[12 * 65], s[13 * 65], s[14 * 65], s[15 * 65]);
;         *(GAS v4u*)(WT + ((size_t)((n0 + n) >> 4) * (K >> 5) + ((k0 + 16 * c) >> 5)) * 512 + ((n0 + n) & 15) * 32 + ((16 * c) & 31)) = o; }
;     LDS_WAIT(); asm volatile("" ::: "memory");
	v_ashrrev_i32_e32 v12, 5, v2
	v_lshlrev_b32_e32 v2, 5, v44
	v_readlane_b32 s18, v253, 54
	v_and_b32_e32 v7, -4, v23
	v_and_b32_e32 v2, 0x1e0, v2
	v_readlane_b32 s19, v253, 55
	v_add3_u32 v46, s82, v6, v7
	v_add_u32_e32 v47, 0x400, v46
	v_lshl_add_u64 v[4:5], s[18:19], 0, v[2:3]
	v_and_b32_e32 v2, 16, v10
	ds_read2_b32 v[10:11], v46 offset1:16
	ds_read2_b32 v[14:15], v46 offset0:65 offset1:81
	ds_read2_b32 v[16:17], v46 offset0:130 offset1:146
	ds_read2_b32 v[18:19], v46 offset0:195 offset1:211
	v_lshl_add_u64 v[4:5], v[4:5], 0, v[2:3]
	ds_read2_b32 v[20:21], v47 offset0:4 offset1:20
	s_waitcnt lgkmcnt(3)
	v_max_f32_e32 v6, v14, v14
	v_max_f32_e32 v2, v10, v10
	v_med3_f32 v7, v6, s95, v199
	s_waitcnt lgkmcnt(2)
	v_max_f32_e32 v6, v16, v16
	v_med3_f32 v2, v2, s95, v199
	v_med3_f32 v8, v6, s95, v199
	v_mov_b32_e32 v6, v3
	v_cvt_pk_fp8_f32 v6, v2, v7
	ds_read2_b32 v[22:23], v47 offset0:69 offset1:85
	ds_read2_b32 v[24:25], v47 offset0:134 offset1:150
	ds_read2_b32 v[26:27], v47 offset0:199 offset1:215
	s_waitcnt lgkmcnt(4)
	v_max_f32_e32 v9, v18, v18
	v_med3_f32 v2, v9, s95, v199
	s_waitcnt lgkmcnt(2)
	v_max_f32_e32 v7, v22, v22
	v_cvt_pk_fp8_f32 v6, v8, v2 op_sel:[0,0,1]
	v_max_f32_e32 v2, v20, v20
	v_med3_f32 v8, v7, s95, v199
	s_waitcnt lgkmcnt(1)
	v_max_f32_e32 v7, v24, v24
	v_add_u32_e32 v48, 0x800, v46
	v_med3_f32 v2, v2, s95, v199
	v_med3_f32 v9, v7, s95, v199
	v_mov_b32_e32 v7, v3
	ds_read2_b32 v[28:29], v48 offset0:8 offset1:24
	v_cvt_pk_fp8_f32 v7, v2, v8
	ds_read2_b32 v[30:31], v48 offset0:73 offset1:89
	ds_read2_b32 v[32:33], v48 offset0:138 offset1:154
	ds_read2_b32 v[34:35], v48 offset0:203 offset1:219
	s_waitcnt lgkmcnt(4)
	v_max_f32_e32 v10, v26, v26
	v_med3_f32 v2, v10, s95, v199
	s_waitcnt lgkmcnt(2)
	v_max_f32_e32 v8, v30, v30
	v_cvt_pk_fp8_f32 v7, v9, v2 op_sel:[0,0,1]
	v_max_f32_e32 v2, v28, v28
	v_med3_f32 v9, v8, s95, v199
	s_waitcnt lgkmcnt(1)
	v_max_f32_e32 v8, v32, v32
	v_add_u32_e32 v49, 0xc00, v46
	v_med3_f32 v2, v2, s95, v199
	v_med3_f32 v10, v8, s95, v199
	v_mov_b32_e32 v8, v3
	ds_read2_b32 v[36:37], v49 offset0:12 offset1:28
	v_cvt_pk_fp8_f32 v8, v2, v9
	ds_read2_b32 v[38:39], v49 offset0:77 offset1:93
	ds_read2_b32 v[40:41], v49 offset0:142 offset1:158
	ds_read2_b32 v[42:43], v49 offset0:207 offset1:223
	s_waitcnt lgkmcnt(4)
	v_max_f32_e32 v14, v34, v34
	v_med3_f32 v2, v14, s95, v199
	v_cvt_pk_fp8_f32 v8, v10, v2 op_sel:[0,0,1]
	s_waitcnt lgkmcnt(3)
	v_max_f32_e32 v2, v36, v36
	s_waitcnt lgkmcnt(2)
	v_max_f32_e32 v9, v38, v38
	v_med3_f32 v2, v2, s95, v199
	v_med3_f32 v10, v9, s95, v199
	v_mov_b32_e32 v9, v3
	v_cvt_pk_fp8_f32 v9, v2, v10
	s_waitcnt lgkmcnt(1)
	v_max_f32_e32 v14, v40, v40
	s_waitcnt lgkmcnt(0)
	v_max_f32_e32 v10, v42, v42
	v_med3_f32 v2, v14, s95, v199
	v_med3_f32 v10, v10, s95, v199
	v_cvt_pk_fp8_f32 v9, v2, v10 op_sel:[0,0,1]
	v_add_u32_e32 v2, s4, v44
	v_ashrrev_i32_e32 v44, 4, v2
	v_ashrrev_i32_e32 v45, 31, v44
	v_ashrrev_i32_e32 v13, 31, v12
	v_lshlrev_b64 v[44:45], 16, v[44:45]
	v_lshlrev_b64 v[12:13], 9, v[12:13]
	v_lshl_add_u64 v[44:45], v[4:5], 0, v[44:45]
	v_lshl_add_u64 v[44:45], v[44:45], 0, v[12:13]
	global_store_dwordx4 v[44:45], v[6:9], off
	v_max_f32_e32 v10, v25, v25
	v_max_f32_e32 v14, v41, v41
	v_max_f32_e32 v6, v11, v11
	v_med3_f32 v7, v6, s95, v199
	v_max_f32_e32 v6, v15, v15
	v_med3_f32 v8, v6, s95, v199
	v_mov_b32_e32 v6, v3
	v_cvt_pk_fp8_f32 v6, v7, v8
	v_max_f32_e32 v9, v17, v17
	v_max_f32_e32 v8, v19, v19
	v_med3_f32 v7, v9, s95, v199
	v_med3_f32 v8, v8, s95, v199
	v_cvt_pk_fp8_f32 v6, v7, v8 op_sel:[0,0,1]
	v_max_f32_e32 v7, v21, v21
	v_med3_f32 v8, v7, s95, v199
	v_max_f32_e32 v7, v23, v23
	v_med3_f32 v9, v7, s95, v199
	v_mov_b32_e32 v7, v3
	v_cvt_pk_fp8_f32 v7, v8, v9
	v_max_f32_e32 v9, v27, v27
	v_med3_f32 v8, v10, s95, v199
	v_med3_f32 v9, v9, s95, v199
	v_cvt_pk_fp8_f32 v7, v8, v9 op_sel:[0,0,1]
	v_max_f32_e32 v8, v29, v29
	v_med3_f32 v9, v8, s95, v199
	v_max_f32_e32 v8, v31, v31
	v_med3_f32 v10, v8, s95, v199
	v_mov_b32_e32 v8, v3
	v_cvt_pk_fp8_f32 v8, v9, v10
	v_max_f32_e32 v11, v33, v33
	v_max_f32_e32 v10, v35, v35
	v_med3_f32 v9, v11, s95, v199
	v_med3_f32 v10, v10, s95, v199
	v_cvt_pk_fp8_f32 v8, v9, v10 op_sel:[0,0,1]
	v_max_f32_e32 v9, v37, v37
	v_med3_f32 v10, v9, s95, v199
	v_max_f32_e32 v9, v39, v39
	v_med3_f32 v11, v9, s95, v199
	v_mov_b32_e32 v9, v3
	v_cvt_pk_fp8_f32 v9, v10, v11
	v_max_f32_e32 v11, v43, v43
	v_med3_f32 v10, v14, s95, v199
	v_med3_f32 v11, v11, s95, v199
	v_cvt_pk_fp8_f32 v9, v10, v11 op_sel:[0,0,1]
	v_add_u32_e32 v10, 16, v2
	v_ashrrev_i32_e32 v10, 4, v10
	v_ashrrev_i32_e32 v11, 31, v10
	v_lshlrev_b64 v[10:11], 16, v[10:11]
	v_lshl_add_u64 v[10:11], v[4:5], 0, v[10:11]
	ds_read2_b32 v[14:15], v46 offset0:32 offset1:48
	v_lshl_add_u64 v[10:11], v[10:11], 0, v[12:13]
	global_store_dwordx4 v[10:11], v[6:9], off
	ds_read2_b32 v[10:11], v46 offset0:97 offset1:113
	ds_read2_b32 v[16:17], v46 offset0:162 offset1:178
	ds_read2_b32 v[18:19], v46 offset0:227 offset1:243
	ds_read2_b32 v[20:21], v47 offset0:36 offset1:52
	s_waitcnt lgkmcnt(4)
; #define GAS __attribute__((address_space(1)))
; #define LAS __attribute__((address_space(3)))
; #define LDS_WAIT() asm volatile("s_waitcnt lgkmcnt(0)" ::: "memory")
;     ...
; #pragma unroll
;     for (int j = 0; j < 4; ++j) { const int n = (lane >> 2) + 16 * j; const LAS float* s = scr + (16 * c) * 65 + n;
;         v4u o; o.x = pg8::pk4_fp8(s[0 * 65], s[1 * 65], s[2 * 65], s[3 * 65]); o.y = pg8::pk4_fp8(s[4 * 65], s[5 * 65], s[6 * 65], s[7 * 65]);
;         o.z = pg8::pk4_fp8(s[8 * 65], s[9 * 65], s[10 * 65], s[11 * 65]); o.w = pg8::pk4_fp8(s[12 * 65], s[13 * 65], s[14 * 65], s[15 * 65]);
;         *(GAS v4u*)(WT + ((size_t)((n0 + n) >> 4) * (K >> 5) + ((k0 + 16 * c) >> 5)) * 512 + ((n0 + n) & 15) * 32 + ((16 * c) & 31)) = o; }
;     LDS_WAIT(); asm volatile("" ::: "memory");
	v_max_f32_e32 v6, v14, v14
	v_med3_f32 v7, v6, s95, v199
	s_waitcnt lgkmcnt(3)
	v_max_f32_e32 v6, v10, v10
	v_med3_f32 v8, v6, s95, v199
	s_waitcnt lgkmcnt(2)
	v_max_f32_e32 v6, v16, v16
	v_med3_f32 v9, v6, s95, v199
	v_mov_b32_e32 v6, v3
	v_cvt_pk_fp8_f32 v6, v7, v8
	s_waitcnt lgkmcnt(1)
	v_max_f32_e32 v7, v18, v18
	ds_read2_b32 v[22:23], v47 offset0:101 offset1:117
	ds_read2_b32 v[24:25], v47 offset0:166 offset1:182
	ds_read2_b32 v[26:27], v47 offset0:231 offset1:247
	v_med3_f32 v7, v7, s95, v199
	v_cvt_pk_fp8_f32 v6, v9, v7 op_sel:[0,0,1]
	s_waitcnt lgkmcnt(3)
	v_max_f32_e32 v7, v20, v20
	v_med3_f32 v8, v7, s95, v199
	s_waitcnt lgkmcnt(2)
	v_max_f32_e32 v7, v22, v22
	v_med3_f32 v9, v7, s95, v199
	s_waitcnt lgkmcnt(1)
	v_max_f32_e32 v7, v24, v24
	v_med3_f32 v10, v7, s95, v199
	v_mov_b32_e32 v7, v3
	ds_read2_b32 v[28:29], v48 offset0:40 offset1:56
	v_cvt_pk_fp8_f32 v7, v8, v9
	s_waitcnt lgkmcnt(1)
	v_max_f32_e32 v8, v26, v26
	ds_read2_b32 v[30:31], v48 offset0:105 offset1:121
	ds_read2_b32 v[32:33], v48 offset0:170 offset1:186
	ds_read2_b32 v[34:35], v48 offset0:235 offset1:251
	v_med3_f32 v8, v8, s95, v199
	v_cvt_pk_fp8_f32 v7, v10, v8 op_sel:[0,0,1]
	s_waitcnt lgkmcnt(3)
	v_max_f32_e32 v8, v28, v28
	v_med3_f32 v9, v8, s95, v199
	s_waitcnt lgkmcnt(2)
	v_max_f32_e32 v8, v30, v30
	v_med3_f32 v10, v8, s95, v199
	s_waitcnt lgkmcnt(1)
	v_max_f32_e32 v8, v32, v32
	v_med3_f32 v14, v8, s95, v199
	v_mov_b32_e32 v8, v3
	ds_read2_b32 v[36:37], v49 offset0:44 offset1:60
	v_cvt_pk_fp8_f32 v8, v9, v10
	s_waitcnt lgkmcnt(1)
	v_max_f32_e32 v9, v34, v34
	ds_read2_b32 v[38:39], v49 offset0:109 offset1:125
	ds_read2_b32 v[40:41], v49 offset0:174 offset1:190
	ds_read2_b32 v[42:43], v49 offset0:239 offset1:255
	v_med3_f32 v9, v9, s95, v199
	v_cvt_pk_fp8_f32 v8, v14, v9 op_sel:[0,0,1]
	s_waitcnt lgkmcnt(3)
	v_max_f32_e32 v9, v36, v36
	v_med3_f32 v10, v9, s95, v199
	s_waitcnt lgkmcnt(2)
	v_max_f32_e32 v9, v38, v38
	v_med3_f32 v14, v9, s95, v199
	v_mov_b32_e32 v9, v3
	v_cvt_pk_fp8_f32 v9, v10, v14
	s_waitcnt lgkmcnt(1)
	v_max_f32_e32 v16, v40, v40
	s_waitcnt lgkmcnt(0)
	v_max_f32_e32 v14, v42, v42
	v_med3_f32 v10, v16, s95, v199
	v_med3_f32 v14, v14, s95, v199
	v_cvt_pk_fp8_f32 v9, v10, v14 op_sel:[0,0,1]
	v_add_u32_e32 v10, 32, v2
	v_ashrrev_i32_e32 v44, 4, v10
	v_ashrrev_i32_e32 v45, 31, v44
	v_lshlrev_b64 v[44:45], 16, v[44:45]
	v_lshl_add_u64 v[44:45], v[4:5], 0, v[44:45]
	v_lshl_add_u64 v[44:45], v[44:45], 0, v[12:13]
	global_store_dwordx4 v[44:45], v[6:9], off
	v_max_f32_e32 v10, v25, v25
	v_max_f32_e32 v14, v41, v41
	v_max_f32_e32 v6, v15, v15
	v_med3_f32 v7, v6, s95, v199
	v_max_f32_e32 v6, v11, v11
	v_med3_f32 v8, v6, s95, v199
	v_mov_b32_e32 v6, v3
	v_cvt_pk_fp8_f32 v6, v7, v8
	v_max_f32_e32 v9, v17, v17
	v_max_f32_e32 v8, v19, v19
	v_med3_f32 v7, v9, s95, v199
	v_med3_f32 v8, v8, s95, v199
	v_cvt_pk_fp8_f32 v6, v7, v8 op_sel:[0,0,1]
	v_max_f32_e32 v7, v21, v21
	v_med3_f32 v8, v7, s95, v199
	v_max_f32_e32 v7, v23, v23
	v_med3_f32 v9, v7, s95, v199
	v_mov_b32_e32 v7, v3
	v_cvt_pk_fp8_f32 v7, v8, v9
	v_max_f32_e32 v9, v27, v27
	v_med3_f32 v8, v10, s95, v199
	v_med3_f32 v9, v9, s95, v199
	v_cvt_pk_fp8_f32 v7, v8, v9 op_sel:[0,0,1]
	v_max_f32_e32 v8, v29, v29
	v_med3_f32 v9, v8, s95, v199
	v_max_f32_e32 v8, v31, v31
	v_med3_f32 v10, v8, s95, v199
	v_mov_b32_e32 v8, v3
	v_cvt_pk_fp8_f32 v8, v9, v10
	v_max_f32_e32 v11, v33, v33
	v_max_f32_e32 v10, v35, v35
	v_med3_f32 v9, v11, s95, v199
	v_med3_f32 v10, v10, s95, v199
	v_cvt_pk_fp8_f32 v8, v9, v10 op_sel:[0,0,1]
	v_max_f32_e32 v9, v37, v37
	v_med3_f32 v10, v9, s95, v199
	v_max_f32_e32 v9, v39, v39
	v_med3_f32 v11, v9, s95, v199
	v_mov_b32_e32 v9, v3
	v_cvt_pk_fp8_f32 v9, v10, v11
	v_max_f32_e32 v11, v43, v43
	v_med3_f32 v10, v14, s95, v199
	v_med3_f32 v11, v11, s95, v199
	v_add_u32_e32 v2, 48, v2
	v_cvt_pk_fp8_f32 v9, v10, v11 op_sel:[0,0,1]
	v_ashrrev_i32_e32 v10, 4, v2
	v_ashrrev_i32_e32 v11, 31, v10
	v_lshlrev_b64 v[10:11], 16, v[10:11]
	v_lshl_add_u64 v[4:5], v[4:5], 0, v[10:11]
	v_lshl_add_u64 v[4:5], v[4:5], 0, v[12:13]
	global_store_dwordx4 v[4:5], v[6:9], off
	s_waitcnt lgkmcnt(0)

; #define PG8_STAGE(bufoff, gbase, voff) do { _Pragma("unroll") for (int _i = 0; _i < 2; ++_i) \
;         __builtin_amdgcn_global_load_lds((const unsigned*)((const char*)(gbase) + (voff)[_i]), (PG8_LAS unsigned*)(lds + (bufoff) + ldsw + _i * 8192), 16, 0, 0); } while (0)
; #define PG8_LDA(dst, b, h) do { _Pragma("unroll") for (int m = 0; m < 4; ++m) _Pragma("unroll") for (int k = 0; k < 2; ++k) dst[m][k] = *(const PG8_LAS bf16x8*)(lds + PG8_SA(b, h) + aoff + m * 2048 + k * 1024); } while (0)
; #define PG8_LDB(dst, b, h) do { _Pragma("unroll") for (int n = 0; n < 2; ++n) _Pragma("unroll") for (int k = 0; k < 2; ++k) dst[n][k] = *(const PG8_LAS bf16x8*)(lds + PG8_SB(b, h) + boff + n * 2048 + k * 1024); } while (0)
; #define PG8_MMA(ai, bj, At, Bt) do { __builtin_amdgcn_s_setprio(1); _Pragma("unroll") for (int m = 0; m < 4; ++m) _Pragma("unroll") for (int n = 0; n < 2; ++n) _Pragma("unroll") for (int k = 0; k < 2; ++k) \
;         acc[ai][bj][m][n] = __builtin_amdgcn_mfma_f32_16x16x32_bf16(Bt[n][k], At[m][k], acc[ai][bj][m][n], 0, 0, 0); __builtin_amdgcn_s_setprio(0); } while (0)
; #define PG8_WAIT_V(n) asm volatile("s_waitcnt vmcnt(" #n ")" ::: "memory")
; #define PG8_WAIT_L(n) asm volatile("s_waitcnt lgkmcnt(" #n ")" ::: "memory")
; #define PG8_BAR __builtin_amdgcn_s_barrier()
; #define PG8_SCHED __builtin_amdgcn_sched_barrier(0)
; #define PG8_BAR __builtin_amdgcn_s_barrier()
; template <class Epi, class Sched, bool ALIGN_EPI = false, bool SP2 = false, bool ABLK = false, bool BBLK = false>
; __device__ __forceinline__ void gemm_phase_f8(PG8_LAS unsigned char* lds, const Gemm g, const Sched& S, const Epi& E) {
;     ...
;             PG8_LDB(B0, 0, 0); PG8_LDB(B1, 0, 1); PG8_SCHED; PG8_LDA(At, 0, 0); PG8_STAGE(PG8_SA(1, 1), a1 + hstep, voffA);
;             PG8_WAIT_V(8); PG8_WAIT_L(0); PG8_BAR; PG8_MMA(0, 0, At, B0); PG8_MMA(0, 1, At, B1); PG8_BAR; PG8_SCHED;
;             PG8_LDA(At, 0, 1); PG8_STAGE(PG8_SB(0, 0), b2, voffB); PG8_STAGE(PG8_SB(0, 1), b2 + hstep, voffB); PG8_STAGE(PG8_SA(0, 0), a2, voffA);
;             PG8_WAIT_V(8); PG8_WAIT_L(0); PG8_BAR; PG8_MMA(1, 0, At, B0); PG8_MMA(1, 1, At, B1); PG8_BAR; PG8_SCHED;
;             PG8_LDB(B0, 1, 0); PG8_LDB(B1, 1, 1); PG8_SCHED; PG8_LDA(At, 1, 0); PG8_STAGE(PG8_SA(0, 1), a2 + hstep, voffA);
;             PG8_WAIT_V(8); PG8_WAIT_L(0); PG8_BAR; PG8_MMA(0, 0, At, B0); PG8_MMA(0, 1, At, B1); PG8_BAR; PG8_SCHED;
.LBB0_2281:
	ds_read_b128 v[18:21], v191
	ds_read_b128 v[22:25], v191 offset:1024
	ds_read_b128 v[26:29], v191 offset:2048
	ds_read_b128 v[30:33], v191 offset:3072
	ds_read_b128 v[2:5], v192
	ds_read_b128 v[6:9], v192 offset:1024
	ds_read_b128 v[10:13], v192 offset:2048
	ds_read_b128 v[14:17], v192 offset:3072
	s_add_u32 s24, s22, 0xfff80080
	s_addc_u32 s25, s23, -1
	s_cmp_eq_u32 s49, 28
	s_cselect_b32 s27, s15, s25
	s_cselect_b32 s26, s45, s24
	s_cselect_b32 s25, s13, s48
	s_cselect_b32 s24, s46, s47
	v_lshl_add_u64 v[212:213], s[22:23], 0, v[174:175]
	s_add_i32 m0, s30, 0xc000
	ds_read_b128 v[182:185], v193
	ds_read_b128 v[186:189], v193 offset:1024
	ds_read_b128 v[196:199], v193 offset:2048
	ds_read_b128 v[200:203], v193 offset:3072
	ds_read_b128 v[204:207], v193 offset:4096
	ds_read_b128 v[208:211], v193 offset:5120
	ds_read_b128 v[218:221], v193 offset:6144
	ds_read_b128 v[222:225], v193 offset:7168
	global_load_lds_dwordx4 v[212:213], off
	v_lshl_add_u64 v[212:213], s[22:23], 0, v[176:177]
	s_add_i32 m0, s30, 0xe000
	s_nop 0
	global_load_lds_dwordx4 v[212:213], off
	s_waitcnt vmcnt(8)
	s_waitcnt lgkmcnt(0)
	s_barrier
	s_setprio 1
	s_waitcnt lgkmcnt(0)
	v_mfma_f32_16x16x128_f8f6f4 v[158:161], v[18:25], v[182:189], v[158:161]
	v_mfma_f32_16x16x128_f8f6f4 v[154:157], v[26:33], v[182:189], v[154:157]
	v_mfma_f32_16x16x128_f8f6f4 v[142:145], v[18:25], v[196:203], v[142:145]
	v_mfma_f32_16x16x128_f8f6f4 v[138:141], v[26:33], v[196:203], v[138:141]
	v_mfma_f32_16x16x128_f8f6f4 v[126:129], v[18:25], v[204:211], v[126:129]
	v_mfma_f32_16x16x128_f8f6f4 v[122:125], v[26:33], v[204:211], v[122:125]
	v_mfma_f32_16x16x128_f8f6f4 v[110:113], v[18:25], v[218:225], v[110:113]
	v_mfma_f32_16x16x128_f8f6f4 v[106:109], v[26:33], v[218:225], v[106:109]
	s_setprio 0
	s_setprio 1
	v_mfma_f32_16x16x128_f8f6f4 v[150:153], v[2:9], v[182:189], v[150:153]
	v_mfma_f32_16x16x128_f8f6f4 v[146:149], v[10:17], v[182:189], v[146:149]
	v_mfma_f32_16x16x128_f8f6f4 v[134:137], v[2:9], v[196:203], v[134:137]
	v_mfma_f32_16x16x128_f8f6f4 v[130:133], v[10:17], v[196:203], v[130:133]
	v_mfma_f32_16x16x128_f8f6f4 v[118:121], v[2:9], v[204:211], v[118:121]
	v_mfma_f32_16x16x128_f8f6f4 v[114:117], v[10:17], v[204:211], v[114:117]
	v_mfma_f32_16x16x128_f8f6f4 v[102:105], v[2:9], v[218:225], v[102:105]
	v_mfma_f32_16x16x128_f8f6f4 v[98:101], v[10:17], v[218:225], v[98:101]
	s_setprio 0
	s_barrier
	s_add_i32 s50, s41, s29
	v_lshl_add_u64 v[182:183], s[24:25], 0, v[164:165]
	s_mov_b32 m0, s50
	ds_read_b128 v[196:199], v193 offset:16384
	ds_read_b128 v[200:203], v193 offset:17408
	ds_read_b128 v[204:207], v193 offset:18432
	ds_read_b128 v[208:211], v193 offset:19456
	ds_read_b128 v[218:221], v193 offset:20480
	ds_read_b128 v[222:225], v193 offset:21504
	ds_read_b128 v[226:229], v193 offset:22528
	ds_read_b128 v[230:233], v193 offset:23552
	global_load_lds_dwordx4 v[182:183], off
	s_add_i32 m0, s50, 0x2000
	s_add_u32 s50, s24, 0x80000
	v_lshl_add_u64 v[184:185], s[24:25], 0, v[168:169]
	s_addc_u32 s51, s25, 0
	s_add_i32 s52, s42, s29
	global_load_lds_dwordx4 v[184:185], off
	v_lshl_add_u64 v[186:187], s[50:51], 0, v[164:165]
	s_mov_b32 m0, s52
	v_lshl_add_u64 v[188:189], s[26:27], 0, v[166:167]
	global_load_lds_dwordx4 v[186:187], off
	v_lshl_add_u64 v[186:187], s[50:51], 0, v[168:169]
	s_add_i32 m0, s52, 0x2000
	s_nop 0
	global_load_lds_dwordx4 v[186:187], off
	v_lshl_add_u64 v[186:187], s[26:27], 0, v[162:163]
	s_mov_b32 m0, s30
	s_nop 0
	global_load_lds_dwordx4 v[186:187], off
	s_mov_b32 m0, s31
	s_nop 0
	global_load_lds_dwordx4 v[188:189], off
	s_waitcnt vmcnt(8)
	s_waitcnt lgkmcnt(0)
	s_barrier
	s_setprio 1
	s_waitcnt lgkmcnt(0)
	v_mfma_f32_16x16x128_f8f6f4 v[94:97], v[18:25], v[196:203], v[94:97]
	v_mfma_f32_16x16x128_f8f6f4 v[90:93], v[26:33], v[196:203], v[90:93]
	v_mfma_f32_16x16x128_f8f6f4 v[78:81], v[18:25], v[204:211], v[78:81]
	v_mfma_f32_16x16x128_f8f6f4 v[74:77], v[26:33], v[204:211], v[74:77]
	v_mfma_f32_16x16x128_f8f6f4 v[62:65], v[18:25], v[218:225], v[62:65]
	v_mfma_f32_16x16x128_f8f6f4 v[58:61], v[26:33], v[218:225], v[58:61]
	v_mfma_f32_16x16x128_f8f6f4 v[46:49], v[18:25], v[226:233], v[46:49]
	v_mfma_f32_16x16x128_f8f6f4 v[42:45], v[26:33], v[226:233], v[42:45]
	s_setprio 0
	s_setprio 1
	v_mfma_f32_16x16x128_f8f6f4 v[86:89], v[2:9], v[196:203], v[86:89]
	v_mfma_f32_16x16x128_f8f6f4 v[82:85], v[10:17], v[196:203], v[82:85]
	v_mfma_f32_16x16x128_f8f6f4 v[70:73], v[2:9], v[204:211], v[70:73]
	v_mfma_f32_16x16x128_f8f6f4 v[66:69], v[10:17], v[204:211], v[66:69]
	v_mfma_f32_16x16x128_f8f6f4 v[54:57], v[2:9], v[218:225], v[54:57]
	v_mfma_f32_16x16x128_f8f6f4 v[50:53], v[10:17], v[218:225], v[50:53]
	v_mfma_f32_16x16x128_f8f6f4 v[38:41], v[2:9], v[226:233], v[38:41]
	v_mfma_f32_16x16x128_f8f6f4 v[34:37], v[10:17], v[226:233], v[34:37]
	s_setprio 0
	s_barrier
	s_add_i32 s50, 0, 0x18000
	s_add_i32 s51, 0, 0x1c000
	v_add_u32_e32 v14, s50, v190
	v_add_u32_e32 v30, s51, v190
	ds_read_b128 v[2:5], v14
	ds_read_b128 v[6:9], v14 offset:1024
	ds_read_b128 v[10:13], v14 offset:2048
	ds_read_b128 v[14:17], v14 offset:3072
	ds_read_b128 v[18:21], v30
	ds_read_b128 v[22:25], v30 offset:1024
	ds_read_b128 v[26:29], v30 offset:2048
	ds_read_b128 v[30:33], v30 offset:3072
	s_add_u32 s26, s26, 0x80000
	s_addc_u32 s27, s27, 0
	s_mov_b32 m0, s33
	v_lshl_add_u64 v[212:213], s[26:27], 0, v[162:163]
	ds_read_b128 v[196:199], v193 offset:32768
	ds_read_b128 v[200:203], v193 offset:33792
	ds_read_b128 v[204:207], v193 offset:34816
	ds_read_b128 v[208:211], v193 offset:35840
	ds_read_b128 v[218:221], v193 offset:36864
	ds_read_b128 v[222:225], v193 offset:37888
	ds_read_b128 v[226:229], v193 offset:38912
	ds_read_b128 v[230:233], v193 offset:39936
	global_load_lds_dwordx4 v[212:213], off
	v_lshl_add_u64 v[212:213], s[26:27], 0, v[166:167]
	s_mov_b32 m0, s34
	s_nop 0
	global_load_lds_dwordx4 v[212:213], off
	s_waitcnt vmcnt(8)
	s_waitcnt lgkmcnt(0)
	s_barrier
; #define PG8_STAGE(bufoff, gbase, voff) do { _Pragma("unroll") for (int _i = 0; _i < 2; ++_i) \
;         __builtin_amdgcn_global_load_lds((const unsigned*)((const char*)(gbase) + (voff)[_i]), (PG8_LAS unsigned*)(lds + (bufoff) + ldsw + _i * 8192), 16, 0, 0); } while (0)
; #define PG8_LDA(dst, b, h) do { _Pragma("unroll") for (int m = 0; m < 4; ++m) _Pragma("unroll") for (int k = 0; k < 2; ++k) dst[m][k] = *(const PG8_LAS bf16x8*)(lds + PG8_SA(b, h) + aoff + m * 2048 + k * 1024); } while (0)
; #define PG8_MMA(ai, bj, At, Bt) do { __builtin_amdgcn_s_setprio(1); _Pragma("unroll") for (int m = 0; m < 4; ++m) _Pragma("unroll") for (int n = 0; n < 2; ++n) _Pragma("unroll") for (int k = 0; k < 2; ++k) \
;         acc[ai][bj][m][n] = __builtin_amdgcn_mfma_f32_16x16x32_bf16(Bt[n][k], At[m][k], acc[ai][bj][m][n], 0, 0, 0); __builtin_amdgcn_s_setprio(0); } while (0)
; #define PG8_WAIT_V(n) asm volatile("s_waitcnt vmcnt(" #n ")" ::: "memory")
; #define PG8_WAIT_L(n) asm volatile("s_waitcnt lgkmcnt(" #n ")" ::: "memory")
; #define PG8_BAR __builtin_amdgcn_s_barrier()
; #define PG8_SCHED __builtin_amdgcn_sched_barrier(0)
; #define PG8_STAGE(bufoff, gbase, voff) do { _Pragma("unroll") for (int _i = 0; _i < 2; ++_i) \
;         __builtin_amdgcn_global_load_lds((const unsigned*)((const char*)(gbase) + (voff)[_i]), (PG8_LAS unsigned*)(lds + (bufoff) + ldsw + _i * 8192), 16, 0, 0); } while (0)
;     __device__ __forceinline__ void operator()(const f32x4 (&acc)[2][2][4][2], const Unit& u, int wr, int wc, int fr, int fq) const {
;     ...
;             for (int m = 0; m < 4; ++m) {
;                 const int row = row0 + ai * HALF + m * 16;
;                 const float rs = rsqrtf(ss[row] * (1.0f / 4096.0f) + RMS_EPS) * (1.0f / 64.0f);
; template <class Epi, class Sched, bool ALIGN_EPI = false, bool SP2 = false, bool ABLK = false, bool BBLK = false>
; __device__ __forceinline__ void gemm_phase_f8(PG8_LAS unsigned char* lds, const Gemm g, const Sched& S, const Epi& E) {
;     ...
;             PG8_WAIT_V(8); PG8_WAIT_L(0); PG8_BAR; PG8_MMA(0, 0, At, B0); PG8_MMA(0, 1, At, B1); PG8_BAR; PG8_SCHED;
;             PG8_LDA(At, 1, 1); PG8_STAGE(PG8_SB(1, 0), b3, voffB); PG8_STAGE(PG8_SB(1, 1), b3 + hstep, voffB); PG8_STAGE(PG8_SA(1, 0), a3, voffA);
;             PG8_WAIT_V(8); PG8_WAIT_L(0); PG8_BAR; PG8_MMA(1, 0, At, B0); PG8_MMA(1, 1, At, B1); PG8_BAR; PG8_SCHED;
	s_setprio 1
	s_waitcnt lgkmcnt(0)
	v_mfma_f32_16x16x128_f8f6f4 v[158:161], v[2:9], v[196:203], v[158:161]
	v_mfma_f32_16x16x128_f8f6f4 v[154:157], v[10:17], v[196:203], v[154:157]
	v_mfma_f32_16x16x128_f8f6f4 v[142:145], v[2:9], v[204:211], v[142:145]
	v_mfma_f32_16x16x128_f8f6f4 v[138:141], v[10:17], v[204:211], v[138:141]
	v_mfma_f32_16x16x128_f8f6f4 v[126:129], v[2:9], v[218:225], v[126:129]
	v_mfma_f32_16x16x128_f8f6f4 v[122:125], v[10:17], v[218:225], v[122:125]
	v_mfma_f32_16x16x128_f8f6f4 v[110:113], v[2:9], v[226:233], v[110:113]
	v_mfma_f32_16x16x128_f8f6f4 v[106:109], v[10:17], v[226:233], v[106:109]
	s_setprio 0
	s_setprio 1
	v_mfma_f32_16x16x128_f8f6f4 v[150:153], v[18:25], v[196:203], v[150:153]
	v_mfma_f32_16x16x128_f8f6f4 v[146:149], v[26:33], v[196:203], v[146:149]
	v_mfma_f32_16x16x128_f8f6f4 v[134:137], v[18:25], v[204:211], v[134:137]
	v_mfma_f32_16x16x128_f8f6f4 v[130:133], v[26:33], v[204:211], v[130:133]
	v_mfma_f32_16x16x128_f8f6f4 v[118:121], v[18:25], v[218:225], v[118:121]
	v_mfma_f32_16x16x128_f8f6f4 v[114:117], v[26:33], v[218:225], v[114:117]
	v_mfma_f32_16x16x128_f8f6f4 v[102:105], v[18:25], v[226:233], v[102:105]
	v_mfma_f32_16x16x128_f8f6f4 v[98:101], v[26:33], v[226:233], v[98:101]
	s_setprio 0
	s_barrier
	s_add_i32 s26, s50, s29
	v_lshl_add_u64 v[182:183], v[182:183], 0, s[6:7]
	s_mov_b32 m0, s26
	ds_read_b128 v[196:199], v193 offset:49152
	ds_read_b128 v[200:203], v193 offset:50176
	ds_read_b128 v[204:207], v193 offset:51200
	ds_read_b128 v[208:211], v193 offset:52224
	ds_read_b128 v[218:221], v193 offset:53248
	ds_read_b128 v[222:225], v193 offset:54272
	ds_read_b128 v[226:229], v193 offset:55296
	ds_read_b128 v[230:233], v193 offset:56320
	global_load_lds_dwordx4 v[182:183], off
	s_add_i32 m0, s26, 0x2000
	s_add_u32 s24, s24, 0x80800
	v_lshl_add_u64 v[182:183], v[184:185], 0, s[6:7]
	s_addc_u32 s25, s25, 0
	s_add_i32 s26, s51, s29
	global_load_lds_dwordx4 v[182:183], off
	v_lshl_add_u64 v[182:183], s[24:25], 0, v[164:165]
	s_mov_b32 m0, s26
	s_nop 0
	global_load_lds_dwordx4 v[182:183], off
	v_lshl_add_u64 v[182:183], s[24:25], 0, v[168:169]
	s_add_i32 m0, s26, 0x2000
	s_nop 0
	global_load_lds_dwordx4 v[182:183], off
	v_lshl_add_u64 v[182:183], v[186:187], 0, s[8:9]
	s_mov_b32 m0, s38
	s_nop 0
	global_load_lds_dwordx4 v[182:183], off
	v_lshl_add_u64 v[182:183], v[188:189], 0, s[8:9]
	s_mov_b32 m0, s39
	s_nop 0
	global_load_lds_dwordx4 v[182:183], off
	s_waitcnt vmcnt(8)
	s_waitcnt lgkmcnt(0)
	s_barrier
	s_setprio 1
	s_waitcnt lgkmcnt(0)
	v_mfma_f32_16x16x128_f8f6f4 v[94:97], v[2:9], v[196:203], v[94:97]
	v_mfma_f32_16x16x128_f8f6f4 v[90:93], v[10:17], v[196:203], v[90:93]
	v_mfma_f32_16x16x128_f8f6f4 v[78:81], v[2:9], v[204:211], v[78:81]
	v_mfma_f32_16x16x128_f8f6f4 v[74:77], v[10:17], v[204:211], v[74:77]
	v_mfma_f32_16x16x128_f8f6f4 v[62:65], v[2:9], v[218:225], v[62:65]
	v_mfma_f32_16x16x128_f8f6f4 v[58:61], v[10:17], v[218:225], v[58:61]
	v_mfma_f32_16x16x128_f8f6f4 v[46:49], v[2:9], v[226:233], v[46:49]
	v_mfma_f32_16x16x128_f8f6f4 v[42:45], v[10:17], v[226:233], v[42:45]
	s_setprio 0
	s_setprio 1
	v_mfma_f32_16x16x128_f8f6f4 v[86:89], v[18:25], v[196:203], v[86:89]
	v_mfma_f32_16x16x128_f8f6f4 v[82:85], v[26:33], v[196:203], v[82:85]
	v_mfma_f32_16x16x128_f8f6f4 v[70:73], v[18:25], v[204:211], v[70:73]
	v_mfma_f32_16x16x128_f8f6f4 v[66:69], v[26:33], v[204:211], v[66:69]
	v_mfma_f32_16x16x128_f8f6f4 v[54:57], v[18:25], v[218:225], v[54:57]
	v_mfma_f32_16x16x128_f8f6f4 v[50:53], v[26:33], v[218:225], v[50:53]
	v_mfma_f32_16x16x128_f8f6f4 v[38:41], v[18:25], v[226:233], v[38:41]
	v_mfma_f32_16x16x128_f8f6f4 v[34:37], v[26:33], v[226:233], v[34:37]
	s_setprio 0
	s_barrier
	s_add_i32 s49, s49, 2
	s_add_u32 s47, s47, 0x1000
	s_addc_u32 s48, s48, 0
	s_add_u32 s22, s22, 0x100
	s_addc_u32 s23, s23, 0
	s_cmp_gt_u32 s49, 29
	s_cbranch_scc0 .LBB0_2281
	s_lshl_b32 s13, s20, 8
	s_add_i32 s13, s13, s36
	v_or_b32_e32 v242, s13, v1
	v_ashrrev_i32_e32 v243, 31, v242
	v_lshl_add_u64 v[244:245], v[242:243], 2, s[2:3]
	global_load_dword v234, v[244:245], off
	global_load_dword v235, v[244:245], off offset:64
	global_load_dword v236, v[244:245], off offset:128
	global_load_dword v237, v[244:245], off offset:192
	global_load_dword v238, v[244:245], off offset:512
	global_load_dword v239, v[244:245], off offset:576
	global_load_dword v240, v[244:245], off offset:640
	global_load_dword v241, v[244:245], off offset:704
	s_and_b64 vcc, exec, s[10:11]
	s_cbranch_vccz .LBB0_2284
	s_barrier
;     __device__ __forceinline__ void operator()(const f32x4 (&acc)[2][2][4][2], const Unit& u, int wr, int wc, int fr, int fq) const {
;         const int row0 = u.pm * BM + wr * 64 + fr, col0 = u.pn * BM + wc * 32 + 8 * fq;
; #pragma unroll
;         for (int ai = 0; ai < 2; ++ai)
; #pragma unroll
;             for (int m = 0; m < 4; ++m) {
;                 const int row = row0 + ai * HALF + m * 16;
;                 const float rs = rsqrtf(ss[row] * (1.0f / 4096.0f) + RMS_EPS) * (1.0f / 64.0f);
;                 unsigned char* rowp = U + ((size_t)(row >> 4) * 512 + (col0 >> 5)) * 512 + (row & 15) * 32 + (col0 & 31);
; #pragma unroll
;                 for (int bj = 0; bj < 2; ++bj) {
;                     f32x4 v0 = acc[ai][bj][m][0] * rs, v1 = acc[ai][bj][m][1] * rs;
; #pragma unroll
;                     for (int j = 0; j < 4; ++j) { const float a = fmaxf(v0[j], 0.f), b = fmaxf(v1[j], 0.f); v0[j] = a * a * 4.f; v1[j] = b * b * 4.f; }
;                     u32x2 w; w.x = pk4_fp8(v0[0], v0[1], v0[2], v0[3]); w.y = pk4_fp8(v1[0], v1[1], v1[2], v1[3]);
;                     *(u32x2*)(rowp + bj * (HALF / 32) * 512) = w;
;                 }
.LBB0_2284:
	s_lshl_b32 s13, s20, 8
	s_add_i32 s13, s13, s36
	v_or_b32_e32 v2, s13, v1
	v_ashrrev_i32_e32 v3, 31, v2
	s_nop 15
	s_nop 15
	v_lshl_add_u64 v[4:5], v[2:3], 2, s[2:3]
	s_lshl_b32 s15, s21, 8
	s_or_b32 s15, s15, s37
	v_mov_b32_e32 v6, 0
	v_mov_b32_e32 v7, 0
	s_ashr_i32 s20, s15, 5
	s_ashr_i32 s22, s13, 4
	v_mov_b32_e32 v8, 0
	s_ashr_i32 s21, s20, 31
	s_ashr_i32 s23, s22, 31
	s_lshl_b64 s[20:21], s[20:21], 9
	s_lshl_b64 s[22:23], s[22:23], 18
	v_readlane_b32 s24, v253, 46
	v_readlane_b32 s25, v253, 47
	s_add_u32 s13, s24, s22
	s_addc_u32 s15, s25, s23
	s_add_u32 s22, s13, s20
	s_addc_u32 s23, s15, s21
	s_waitcnt vmcnt(0)
	v_fmamk_f32 v3, v234, 0x39800000, v194
	v_mul_f32_e32 v9, 0x4b800000, v3
	v_cmp_gt_f32_e32 vcc, s43, v3
	s_nop 1
	v_cndmask_b32_e32 v3, v3, v9, vcc
	v_rsq_f32_e32 v3, v3
	s_nop 0
	v_mul_f32_e32 v9, 0x45800000, v3
	v_cndmask_b32_e32 v3, v3, v9, vcc
	v_mul_f32_e32 v10, 0x3c800000, v3
	v_pk_mul_f32 v[14:15], v[158:159], v[10:11] op_sel_hi:[1,0]
	v_pk_mul_f32 v[18:19], v[154:155], v[10:11] op_sel_hi:[1,0]
	v_pk_mul_f32 v[12:13], v[160:161], v[10:11] op_sel_hi:[1,0]
	v_pk_mul_f32 v[16:17], v[156:157], v[10:11] op_sel_hi:[1,0]
	v_pk_mul_f32 v[20:21], v[152:153], v[10:11] op_sel_hi:[1,0]
	v_pk_mul_f32 v[22:23], v[150:151], v[10:11] op_sel_hi:[1,0]
	v_pk_mul_f32 v[24:25], v[148:149], v[10:11] op_sel_hi:[1,0]
	v_pk_mul_f32 v[10:11], v[146:147], v[10:11] op_sel_hi:[1,0]
	v_max_f32_e32 v3, 0, v14
	v_max_f32_e32 v9, 0, v18
	v_max_f32_e32 v14, 0, v15
	v_max_f32_e32 v15, 0, v19
	v_max_f32_e32 v18, 0, v22
	v_max_f32_e32 v10, 0, v10
	v_max_f32_e32 v19, 0, v23
	v_max_f32_e32 v11, 0, v11
	v_mul_f32_e32 v3, v3, v3
	v_mul_f32_e32 v9, v9, v9
	v_mul_f32_e32 v14, v14, v14
	v_mul_f32_e32 v15, v15, v15
	v_mul_f32_e32 v18, v18, v18
	v_mul_f32_e32 v10, v10, v10
	v_mul_f32_e32 v19, v19, v19
	v_mul_f32_e32 v11, v11, v11
	v_mul_f32_e32 v3, 4.0, v3
	v_mul_f32_e32 v9, 4.0, v9
	v_mul_f32_e32 v14, 4.0, v14
	v_mul_f32_e32 v15, 4.0, v15
	v_mul_f32_e32 v18, 4.0, v18
	v_mul_f32_e32 v10, 4.0, v10
	v_mul_f32_e32 v19, 4.0, v19
	v_mul_f32_e32 v11, 4.0, v11
	v_med3_f32 v3, v3, s44, v195
	v_med3_f32 v14, v14, s44, v195
	v_med3_f32 v9, v9, s44, v195
	v_med3_f32 v15, v15, s44, v195
	v_max_f32_e32 v12, 0, v12
	v_max_f32_e32 v16, 0, v16
	v_max_f32_e32 v13, 0, v13
	v_max_f32_e32 v17, 0, v17
	v_med3_f32 v18, v18, s44, v195
	v_med3_f32 v19, v19, s44, v195
	v_med3_f32 v10, v10, s44, v195
	v_cvt_pk_fp8_f32 v6, v3, v14
	v_cvt_pk_fp8_f32 v7, v9, v15
	v_med3_f32 v3, v11, s44, v195
	v_mov_b32_e32 v9, 0
	v_max_f32_e32 v20, 0, v20
	v_max_f32_e32 v22, 0, v24
	v_max_f32_e32 v21, 0, v21
	v_max_f32_e32 v23, 0, v25
	v_mul_f32_e32 v12, v12, v12
	v_mul_f32_e32 v16, v16, v16
	v_mul_f32_e32 v13, v13, v13
	v_mul_f32_e32 v17, v17, v17
	v_cvt_pk_fp8_f32 v8, v18, v19
	v_cvt_pk_fp8_f32 v9, v10, v3
	v_mul_f32_e32 v20, v20, v20
	v_mul_f32_e32 v22, v22, v22
	v_mul_f32_e32 v21, v21, v21
	v_mul_f32_e32 v23, v23, v23
	v_mul_f32_e32 v12, 4.0, v12
	v_mul_f32_e32 v16, 4.0, v16
	v_mul_f32_e32 v13, 4.0, v13
	v_mul_f32_e32 v17, 4.0, v17
	v_mul_f32_e32 v20, 4.0, v20
	v_mul_f32_e32 v22, 4.0, v22
	v_mul_f32_e32 v21, 4.0, v21
	v_mul_f32_e32 v23, 4.0, v23
	v_med3_f32 v12, v12, s44, v195
	v_med3_f32 v13, v13, s44, v195
	v_med3_f32 v16, v16, s44, v195
	v_med3_f32 v17, v17, s44, v195
	v_med3_f32 v20, v20, s44, v195
	v_med3_f32 v21, v21, s44, v195
	v_cvt_pk_fp8_f32 v6, v12, v13 op_sel:[0,0,1]
	v_cvt_pk_fp8_f32 v7, v16, v17 op_sel:[0,0,1]
	v_med3_f32 v3, v22, s44, v195
	v_med3_f32 v10, v23, s44, v195
	v_cvt_pk_fp8_f32 v8, v20, v21 op_sel:[0,0,1]
	v_cvt_pk_fp8_f32 v9, v3, v10 op_sel:[0,0,1]
	v_lshl_add_u64 v[10:11], s[22:23], 0, v[172:173]
	v_lshl_add_u64 v[10:11], v[10:11], 0, v[170:171]
	global_store_dwordx2 v[10:11], v[6:7], off
	global_store_dwordx2 v[10:11], v[8:9], off offset:2048
	v_or_b32_e32 v6, 16, v2
	v_ashrrev_i32_e32 v7, 31, v6
	v_lshl_add_u64 v[8:9], v[6:7], 2, s[2:3]
	v_mov_b32_e32 v8, 0
	v_mov_b32_e32 v9, 0
	v_mov_b32_e32 v10, 0
	v_ashrrev_i32_e32 v6, 4, v6
	v_ashrrev_i32_e32 v7, 31, v6
	v_lshlrev_b64 v[6:7], 18, v[6:7]
	v_lshl_add_u64 v[6:7], s[24:25], 0, v[6:7]
	v_lshl_add_u64 v[6:7], v[6:7], 0, s[20:21]
	v_lshl_add_u64 v[6:7], v[6:7], 0, v[172:173]
	v_lshl_add_u64 v[6:7], v[6:7], 0, v[170:171]
	v_fmamk_f32 v3, v235, 0x39800000, v194
	v_mul_f32_e32 v11, 0x4b800000, v3
	v_cmp_gt_f32_e32 vcc, s43, v3
	s_nop 1
	v_cndmask_b32_e32 v3, v3, v11, vcc
	v_rsq_f32_e32 v3, v3
	s_nop 0
	v_mul_f32_e32 v11, 0x45800000, v3
	v_cndmask_b32_e32 v3, v3, v11, vcc
	v_mul_f32_e32 v12, 0x3c800000, v3
	v_pk_mul_f32 v[16:17], v[142:143], v[12:13] op_sel_hi:[1,0]
	v_pk_mul_f32 v[20:21], v[138:139], v[12:13] op_sel_hi:[1,0]
	v_pk_mul_f32 v[14:15], v[144:145], v[12:13] op_sel_hi:[1,0]
	v_pk_mul_f32 v[18:19], v[140:141], v[12:13] op_sel_hi:[1,0]
	v_pk_mul_f32 v[22:23], v[136:137], v[12:13] op_sel_hi:[1,0]
	v_pk_mul_f32 v[24:25], v[134:135], v[12:13] op_sel_hi:[1,0]
	v_pk_mul_f32 v[26:27], v[132:133], v[12:13] op_sel_hi:[1,0]
	v_pk_mul_f32 v[12:13], v[130:131], v[12:13] op_sel_hi:[1,0]
	v_max_f32_e32 v3, 0, v16
	v_max_f32_e32 v11, 0, v20
	v_max_f32_e32 v16, 0, v17
	v_max_f32_e32 v17, 0, v21
	v_max_f32_e32 v20, 0, v24
	v_max_f32_e32 v12, 0, v12
	v_max_f32_e32 v21, 0, v25
	v_max_f32_e32 v13, 0, v13
	v_mul_f32_e32 v3, v3, v3
	v_mul_f32_e32 v11, v11, v11
	v_mul_f32_e32 v16, v16, v16
	v_mul_f32_e32 v17, v17, v17
	v_mul_f32_e32 v20, v20, v20
	v_mul_f32_e32 v12, v12, v12
	v_mul_f32_e32 v21, v21, v21
	v_mul_f32_e32 v13, v13, v13
	v_mul_f32_e32 v3, 4.0, v3
	v_mul_f32_e32 v11, 4.0, v11
	v_mul_f32_e32 v16, 4.0, v16
	v_mul_f32_e32 v17, 4.0, v17
	v_mul_f32_e32 v20, 4.0, v20
	v_mul_f32_e32 v12, 4.0, v12
	v_mul_f32_e32 v21, 4.0, v21
;     __device__ __forceinline__ void operator()(const f32x4 (&acc)[2][2][4][2], const Unit& u, int wr, int wc, int fr, int fq) const {
;         const int row0 = u.pm * BM + wr * 64 + fr, col0 = u.pn * BM + wc * 32 + 8 * fq;
; #pragma unroll
;         for (int ai = 0; ai < 2; ++ai)
; #pragma unroll
;             for (int m = 0; m < 4; ++m) {
;                 const int row = row0 + ai * HALF + m * 16;
;                 const float rs = rsqrtf(ss[row] * (1.0f / 4096.0f) + RMS_EPS) * (1.0f / 64.0f);
;                 unsigned char* rowp = U + ((size_t)(row >> 4) * 512 + (col0 >> 5)) * 512 + (row & 15) * 32 + (col0 & 31);
; #pragma unroll
;                 for (int bj = 0; bj < 2; ++bj) {
;                     f32x4 v0 = acc[ai][bj][m][0] * rs, v1 = acc[ai][bj][m][1] * rs;
; #pragma unroll
;                     for (int j = 0; j < 4; ++j) { const float a = fmaxf(v0[j], 0.f), b = fmaxf(v1[j], 0.f); v0[j] = a * a * 4.f; v1[j] = b * b * 4.f; }
;                     u32x2 w; w.x = pk4_fp8(v0[0], v0[1], v0[2], v0[3]); w.y = pk4_fp8(v1[0], v1[1], v1[2], v1[3]);
;                     *(u32x2*)(rowp + bj * (HALF / 32) * 512) = w;
;                 }
	v_mul_f32_e32 v13, 4.0, v13
	v_med3_f32 v3, v3, s44, v195
	v_med3_f32 v16, v16, s44, v195
	v_med3_f32 v11, v11, s44, v195
	v_med3_f32 v17, v17, s44, v195
	v_max_f32_e32 v14, 0, v14
	v_max_f32_e32 v18, 0, v18
	v_max_f32_e32 v15, 0, v15
	v_max_f32_e32 v19, 0, v19
	v_med3_f32 v20, v20, s44, v195
	v_med3_f32 v21, v21, s44, v195
	v_cvt_pk_fp8_f32 v8, v3, v16
	v_cvt_pk_fp8_f32 v9, v11, v17
	v_med3_f32 v3, v12, s44, v195
	v_med3_f32 v12, v13, s44, v195
	v_mov_b32_e32 v11, 0
	v_max_f32_e32 v22, 0, v22
	v_max_f32_e32 v24, 0, v26
	v_max_f32_e32 v23, 0, v23
	v_max_f32_e32 v25, 0, v27
	v_mul_f32_e32 v14, v14, v14
	v_mul_f32_e32 v18, v18, v18
	v_mul_f32_e32 v15, v15, v15
	v_mul_f32_e32 v19, v19, v19
	v_cvt_pk_fp8_f32 v10, v20, v21
	v_cvt_pk_fp8_f32 v11, v3, v12
	v_mul_f32_e32 v22, v22, v22
	v_mul_f32_e32 v24, v24, v24
	v_mul_f32_e32 v23, v23, v23
	v_mul_f32_e32 v25, v25, v25
	v_mul_f32_e32 v14, 4.0, v14
	v_mul_f32_e32 v18, 4.0, v18
	v_mul_f32_e32 v15, 4.0, v15
	v_mul_f32_e32 v19, 4.0, v19
	v_mul_f32_e32 v22, 4.0, v22
	v_mul_f32_e32 v24, 4.0, v24
	v_mul_f32_e32 v23, 4.0, v23
	v_mul_f32_e32 v25, 4.0, v25
	v_med3_f32 v14, v14, s44, v195
	v_med3_f32 v15, v15, s44, v195
	v_med3_f32 v18, v18, s44, v195
	v_med3_f32 v19, v19, s44, v195
	v_med3_f32 v22, v22, s44, v195
	v_med3_f32 v23, v23, s44, v195
	v_cvt_pk_fp8_f32 v8, v14, v15 op_sel:[0,0,1]
	v_cvt_pk_fp8_f32 v9, v18, v19 op_sel:[0,0,1]
	v_med3_f32 v3, v24, s44, v195
	v_med3_f32 v12, v25, s44, v195
	v_cvt_pk_fp8_f32 v10, v22, v23 op_sel:[0,0,1]
	v_cvt_pk_fp8_f32 v11, v3, v12 op_sel:[0,0,1]
	global_store_dwordx2 v[6:7], v[8:9], off
	global_store_dwordx2 v[6:7], v[10:11], off offset:2048
	v_or_b32_e32 v6, 32, v2
	v_ashrrev_i32_e32 v7, 31, v6
	v_lshl_add_u64 v[8:9], v[6:7], 2, s[2:3]
	v_mov_b32_e32 v8, 0
	v_mov_b32_e32 v9, 0
	v_mov_b32_e32 v10, 0
	v_ashrrev_i32_e32 v6, 4, v6
	v_ashrrev_i32_e32 v7, 31, v6
	v_lshlrev_b64 v[6:7], 18, v[6:7]
	v_lshl_add_u64 v[6:7], s[24:25], 0, v[6:7]
	v_lshl_add_u64 v[6:7], v[6:7], 0, s[20:21]
	v_lshl_add_u64 v[6:7], v[6:7], 0, v[172:173]
	v_lshl_add_u64 v[6:7], v[6:7], 0, v[170:171]
	v_fmamk_f32 v3, v236, 0x39800000, v194
	v_mul_f32_e32 v11, 0x4b800000, v3
	v_cmp_gt_f32_e32 vcc, s43, v3
	s_nop 1
	v_cndmask_b32_e32 v3, v3, v11, vcc
	v_rsq_f32_e32 v3, v3
	s_nop 0
	v_mul_f32_e32 v11, 0x45800000, v3
	v_cndmask_b32_e32 v3, v3, v11, vcc
	v_mul_f32_e32 v12, 0x3c800000, v3
	v_pk_mul_f32 v[16:17], v[126:127], v[12:13] op_sel_hi:[1,0]
	v_pk_mul_f32 v[20:21], v[122:123], v[12:13] op_sel_hi:[1,0]
	v_pk_mul_f32 v[24:25], v[118:119], v[12:13] op_sel_hi:[1,0]
	v_pk_mul_f32 v[14:15], v[128:129], v[12:13] op_sel_hi:[1,0]
	v_pk_mul_f32 v[18:19], v[124:125], v[12:13] op_sel_hi:[1,0]
	v_pk_mul_f32 v[22:23], v[120:121], v[12:13] op_sel_hi:[1,0]
	v_pk_mul_f32 v[26:27], v[116:117], v[12:13] op_sel_hi:[1,0]
	v_pk_mul_f32 v[12:13], v[114:115], v[12:13] op_sel_hi:[1,0]
	v_max_f32_e32 v3, 0, v16
	v_max_f32_e32 v11, 0, v20
	v_max_f32_e32 v16, 0, v17
	v_max_f32_e32 v17, 0, v21
	v_max_f32_e32 v20, 0, v24
	v_max_f32_e32 v21, 0, v25
	v_max_f32_e32 v12, 0, v12
	v_max_f32_e32 v13, 0, v13
	v_mul_f32_e32 v3, v3, v3
	v_mul_f32_e32 v11, v11, v11
	v_mul_f32_e32 v16, v16, v16
	v_mul_f32_e32 v17, v17, v17
	v_mul_f32_e32 v20, v20, v20
	v_mul_f32_e32 v21, v21, v21
	v_mul_f32_e32 v12, v12, v12
	v_mul_f32_e32 v13, v13, v13
	v_mul_f32_e32 v3, 4.0, v3
	v_mul_f32_e32 v11, 4.0, v11
	v_mul_f32_e32 v16, 4.0, v16
	v_mul_f32_e32 v17, 4.0, v17
	v_mul_f32_e32 v20, 4.0, v20
	v_mul_f32_e32 v21, 4.0, v21
	v_mul_f32_e32 v12, 4.0, v12
	v_mul_f32_e32 v13, 4.0, v13
	v_med3_f32 v3, v3, s44, v195
	v_med3_f32 v16, v16, s44, v195
	v_med3_f32 v11, v11, s44, v195
	v_med3_f32 v17, v17, s44, v195
	v_med3_f32 v20, v20, s44, v195
	v_med3_f32 v21, v21, s44, v195
	v_max_f32_e32 v14, 0, v14
	v_max_f32_e32 v18, 0, v18
	v_max_f32_e32 v15, 0, v15
	v_max_f32_e32 v19, 0, v19
	v_max_f32_e32 v22, 0, v22
	v_max_f32_e32 v23, 0, v23
	v_cvt_pk_fp8_f32 v8, v3, v16
	v_cvt_pk_fp8_f32 v9, v11, v17
	v_cvt_pk_fp8_f32 v10, v20, v21
	v_med3_f32 v12, v12, s44, v195
	v_med3_f32 v13, v13, s44, v195
	v_mov_b32_e32 v11, 0
	v_max_f32_e32 v24, 0, v26
	v_max_f32_e32 v25, 0, v27
	v_mul_f32_e32 v14, v14, v14
	v_mul_f32_e32 v18, v18, v18
	v_mul_f32_e32 v15, v15, v15
	v_mul_f32_e32 v19, v19, v19
	v_mul_f32_e32 v22, v22, v22
	v_mul_f32_e32 v23, v23, v23
	v_cvt_pk_fp8_f32 v11, v12, v13
	v_mul_f32_e32 v24, v24, v24
	v_mul_f32_e32 v25, v25, v25
	v_mul_f32_e32 v14, 4.0, v14
	v_mul_f32_e32 v18, 4.0, v18
	v_mul_f32_e32 v15, 4.0, v15
	v_mul_f32_e32 v19, 4.0, v19
	v_mul_f32_e32 v22, 4.0, v22
	v_mul_f32_e32 v23, 4.0, v23
	v_mul_f32_e32 v24, 4.0, v24
	v_mul_f32_e32 v25, 4.0, v25
	v_med3_f32 v14, v14, s44, v195
	v_med3_f32 v15, v15, s44, v195
	v_med3_f32 v18, v18, s44, v195
	v_med3_f32 v19, v19, s44, v195
	v_med3_f32 v22, v22, s44, v195
	v_med3_f32 v3, v23, s44, v195
	v_cvt_pk_fp8_f32 v8, v14, v15 op_sel:[0,0,1]
	v_cvt_pk_fp8_f32 v9, v18, v19 op_sel:[0,0,1]
	v_cvt_pk_fp8_f32 v10, v22, v3 op_sel:[0,0,1]
	v_med3_f32 v3, v24, s44, v195
	v_med3_f32 v12, v25, s44, v195
	v_cvt_pk_fp8_f32 v11, v3, v12 op_sel:[0,0,1]
	global_store_dwordx2 v[6:7], v[8:9], off
	global_store_dwordx2 v[6:7], v[10:11], off offset:2048
	v_or_b32_e32 v6, 48, v2
	v_ashrrev_i32_e32 v7, 31, v6
	v_lshl_add_u64 v[8:9], v[6:7], 2, s[2:3]
	v_mov_b32_e32 v8, 0
	v_mov_b32_e32 v9, 0
	v_mov_b32_e32 v10, 0
	v_ashrrev_i32_e32 v6, 4, v6
	v_ashrrev_i32_e32 v7, 31, v6
	v_lshlrev_b64 v[6:7], 18, v[6:7]
	v_lshl_add_u64 v[6:7], s[24:25], 0, v[6:7]
	v_lshl_add_u64 v[6:7], v[6:7], 0, s[20:21]
	v_lshl_add_u64 v[6:7], v[6:7], 0, v[172:173]
	v_lshl_add_u64 v[6:7], v[6:7], 0, v[170:171]
	v_fmamk_f32 v3, v237, 0x39800000, v194
	v_mul_f32_e32 v11, 0x4b800000, v3
;     __device__ __forceinline__ void operator()(const f32x4 (&acc)[2][2][4][2], const Unit& u, int wr, int wc, int fr, int fq) const {
;         const int row0 = u.pm * BM + wr * 64 + fr, col0 = u.pn * BM + wc * 32 + 8 * fq;
; #pragma unroll
;         for (int ai = 0; ai < 2; ++ai)
; #pragma unroll
;             for (int m = 0; m < 4; ++m) {
;                 const int row = row0 + ai * HALF + m * 16;
;                 const float rs = rsqrtf(ss[row] * (1.0f / 4096.0f) + RMS_EPS) * (1.0f / 64.0f);
;                 unsigned char* rowp = U + ((size_t)(row >> 4) * 512 + (col0 >> 5)) * 512 + (row & 15) * 32 + (col0 & 31);
; #pragma unroll
;                 for (int bj = 0; bj < 2; ++bj) {
;                     f32x4 v0 = acc[ai][bj][m][0] * rs, v1 = acc[ai][bj][m][1] * rs;
; #pragma unroll
;                     for (int j = 0; j < 4; ++j) { const float a = fmaxf(v0[j], 0.f), b = fmaxf(v1[j], 0.f); v0[j] = a * a * 4.f; v1[j] = b * b * 4.f; }
;                     u32x2 w; w.x = pk4_fp8(v0[0], v0[1], v0[2], v0[3]); w.y = pk4_fp8(v1[0], v1[1], v1[2], v1[3]);
;                     *(u32x2*)(rowp + bj * (HALF / 32) * 512) = w;
;                 }
	v_cmp_gt_f32_e32 vcc, s43, v3
	s_nop 1
	v_cndmask_b32_e32 v3, v3, v11, vcc
	v_rsq_f32_e32 v3, v3
	s_nop 0
	v_mul_f32_e32 v11, 0x45800000, v3
	v_cndmask_b32_e32 v3, v3, v11, vcc
	v_mul_f32_e32 v12, 0x3c800000, v3
	v_pk_mul_f32 v[16:17], v[110:111], v[12:13] op_sel_hi:[1,0]
	v_pk_mul_f32 v[20:21], v[106:107], v[12:13] op_sel_hi:[1,0]
	v_pk_mul_f32 v[24:25], v[102:103], v[12:13] op_sel_hi:[1,0]
	v_pk_mul_f32 v[14:15], v[112:113], v[12:13] op_sel_hi:[1,0]
	v_pk_mul_f32 v[18:19], v[108:109], v[12:13] op_sel_hi:[1,0]
	v_pk_mul_f32 v[22:23], v[104:105], v[12:13] op_sel_hi:[1,0]
	v_pk_mul_f32 v[26:27], v[100:101], v[12:13] op_sel_hi:[1,0]
	v_pk_mul_f32 v[12:13], v[98:99], v[12:13] op_sel_hi:[1,0]
	v_max_f32_e32 v3, 0, v16
	v_max_f32_e32 v11, 0, v20
	v_max_f32_e32 v16, 0, v17
	v_max_f32_e32 v17, 0, v21
	v_max_f32_e32 v20, 0, v24
	v_max_f32_e32 v21, 0, v25
	v_max_f32_e32 v12, 0, v12
	v_max_f32_e32 v13, 0, v13
	v_mul_f32_e32 v3, v3, v3
	v_mul_f32_e32 v11, v11, v11
	v_mul_f32_e32 v16, v16, v16
	v_mul_f32_e32 v17, v17, v17
	v_mul_f32_e32 v20, v20, v20
	v_mul_f32_e32 v21, v21, v21
	v_mul_f32_e32 v12, v12, v12
	v_mul_f32_e32 v13, v13, v13
	v_mul_f32_e32 v3, 4.0, v3
	v_mul_f32_e32 v11, 4.0, v11
	v_mul_f32_e32 v16, 4.0, v16
	v_mul_f32_e32 v17, 4.0, v17
	v_mul_f32_e32 v20, 4.0, v20
	v_mul_f32_e32 v21, 4.0, v21
	v_mul_f32_e32 v12, 4.0, v12
	v_mul_f32_e32 v13, 4.0, v13
	v_med3_f32 v3, v3, s44, v195
	v_med3_f32 v16, v16, s44, v195
	v_med3_f32 v11, v11, s44, v195
	v_med3_f32 v17, v17, s44, v195
	v_med3_f32 v20, v20, s44, v195
	v_med3_f32 v21, v21, s44, v195
	v_max_f32_e32 v14, 0, v14
	v_max_f32_e32 v18, 0, v18
	v_max_f32_e32 v15, 0, v15
	v_max_f32_e32 v19, 0, v19
	v_max_f32_e32 v22, 0, v22
	v_max_f32_e32 v23, 0, v23
	v_cvt_pk_fp8_f32 v8, v3, v16
	v_cvt_pk_fp8_f32 v9, v11, v17
	v_cvt_pk_fp8_f32 v10, v20, v21
	v_med3_f32 v12, v12, s44, v195
	v_med3_f32 v13, v13, s44, v195
	v_mov_b32_e32 v11, 0
	v_max_f32_e32 v24, 0, v26
	v_max_f32_e32 v25, 0, v27
	v_mul_f32_e32 v14, v14, v14
	v_mul_f32_e32 v18, v18, v18
	v_mul_f32_e32 v15, v15, v15
	v_mul_f32_e32 v19, v19, v19
	v_mul_f32_e32 v22, v22, v22
	v_mul_f32_e32 v23, v23, v23
	v_cvt_pk_fp8_f32 v11, v12, v13
	v_mul_f32_e32 v24, v24, v24
	v_mul_f32_e32 v25, v25, v25
	v_mul_f32_e32 v14, 4.0, v14
	v_mul_f32_e32 v18, 4.0, v18
	v_mul_f32_e32 v15, 4.0, v15
	v_mul_f32_e32 v19, 4.0, v19
	v_mul_f32_e32 v22, 4.0, v22
	v_mul_f32_e32 v23, 4.0, v23
	v_mul_f32_e32 v24, 4.0, v24
	v_mul_f32_e32 v25, 4.0, v25
	v_med3_f32 v14, v14, s44, v195
	v_med3_f32 v15, v15, s44, v195
	v_med3_f32 v18, v18, s44, v195
	v_med3_f32 v19, v19, s44, v195
	v_med3_f32 v3, v22, s44, v195
	v_med3_f32 v16, v23, s44, v195
	v_cvt_pk_fp8_f32 v8, v14, v15 op_sel:[0,0,1]
	v_cvt_pk_fp8_f32 v9, v18, v19 op_sel:[0,0,1]
	v_cvt_pk_fp8_f32 v10, v3, v16 op_sel:[0,0,1]
	v_med3_f32 v3, v24, s44, v195
	v_med3_f32 v12, v25, s44, v195
	v_cvt_pk_fp8_f32 v11, v3, v12 op_sel:[0,0,1]
	global_store_dwordx2 v[6:7], v[8:9], off
	global_store_dwordx2 v[6:7], v[10:11], off offset:2048
	v_add_u32_e32 v9, 0x80, v2
	v_ashrrev_i32_e32 v10, 4, v9
	v_mov_b32_e32 v6, 0
	v_mov_b32_e32 v7, 0
	v_mov_b32_e32 v8, 0
	v_ashrrev_i32_e32 v11, 31, v10
	v_lshlrev_b64 v[10:11], 18, v[10:11]
	v_lshl_add_u64 v[10:11], s[24:25], 0, v[10:11]
	v_lshl_add_u64 v[10:11], v[10:11], 0, s[20:21]
	v_lshl_add_u64 v[10:11], v[10:11], 0, v[172:173]
	v_lshl_add_u64 v[10:11], v[10:11], 0, v[170:171]
	v_fmamk_f32 v3, v238, 0x39800000, v194
	v_mul_f32_e32 v9, 0x4b800000, v3
	v_cmp_gt_f32_e32 vcc, s43, v3
	s_nop 1
	v_cndmask_b32_e32 v3, v3, v9, vcc
	v_rsq_f32_e32 v3, v3
	s_nop 0
	v_mul_f32_e32 v9, 0x45800000, v3
	v_cndmask_b32_e32 v3, v3, v9, vcc
	v_mul_f32_e32 v12, 0x3c800000, v3
	v_pk_mul_f32 v[16:17], v[94:95], v[12:13] op_sel_hi:[1,0]
	v_pk_mul_f32 v[20:21], v[90:91], v[12:13] op_sel_hi:[1,0]
	v_pk_mul_f32 v[24:25], v[86:87], v[12:13] op_sel_hi:[1,0]
	v_pk_mul_f32 v[14:15], v[96:97], v[12:13] op_sel_hi:[1,0]
	v_pk_mul_f32 v[18:19], v[92:93], v[12:13] op_sel_hi:[1,0]
	v_pk_mul_f32 v[22:23], v[88:89], v[12:13] op_sel_hi:[1,0]
	v_pk_mul_f32 v[26:27], v[84:85], v[12:13] op_sel_hi:[1,0]
	v_pk_mul_f32 v[12:13], v[82:83], v[12:13] op_sel_hi:[1,0]
	v_max_f32_e32 v3, 0, v16
	v_max_f32_e32 v9, 0, v20
	v_max_f32_e32 v16, 0, v17
	v_max_f32_e32 v17, 0, v21
	v_max_f32_e32 v20, 0, v24
	v_max_f32_e32 v21, 0, v25
	v_max_f32_e32 v12, 0, v12
	v_max_f32_e32 v13, 0, v13
	v_mul_f32_e32 v3, v3, v3
	v_mul_f32_e32 v9, v9, v9
	v_mul_f32_e32 v16, v16, v16
	v_mul_f32_e32 v17, v17, v17
	v_mul_f32_e32 v20, v20, v20
	v_mul_f32_e32 v21, v21, v21
	v_mul_f32_e32 v12, v12, v12
	v_mul_f32_e32 v13, v13, v13
	v_mul_f32_e32 v3, 4.0, v3
	v_mul_f32_e32 v9, 4.0, v9
	v_mul_f32_e32 v16, 4.0, v16
	v_mul_f32_e32 v17, 4.0, v17
	v_mul_f32_e32 v20, 4.0, v20
	v_mul_f32_e32 v21, 4.0, v21
	v_mul_f32_e32 v12, 4.0, v12
	v_mul_f32_e32 v13, 4.0, v13
	v_med3_f32 v3, v3, s44, v195
	v_med3_f32 v16, v16, s44, v195
	v_med3_f32 v9, v9, s44, v195
	v_med3_f32 v17, v17, s44, v195
	v_med3_f32 v20, v20, s44, v195
	v_med3_f32 v21, v21, s44, v195
	v_max_f32_e32 v14, 0, v14
	v_max_f32_e32 v18, 0, v18
	v_max_f32_e32 v15, 0, v15
	v_max_f32_e32 v19, 0, v19
	v_max_f32_e32 v22, 0, v22
	v_max_f32_e32 v23, 0, v23
	v_cvt_pk_fp8_f32 v6, v3, v16
	v_cvt_pk_fp8_f32 v7, v9, v17
	v_cvt_pk_fp8_f32 v8, v20, v21
	v_med3_f32 v12, v12, s44, v195
	v_med3_f32 v13, v13, s44, v195
	v_mov_b32_e32 v9, 0
	v_max_f32_e32 v24, 0, v26
	v_max_f32_e32 v25, 0, v27
	v_mul_f32_e32 v14, v14, v14
	v_mul_f32_e32 v18, v18, v18
	v_mul_f32_e32 v15, v15, v15
	v_mul_f32_e32 v19, v19, v19
	v_mul_f32_e32 v22, v22, v22
	v_mul_f32_e32 v23, v23, v23
	v_cvt_pk_fp8_f32 v9, v12, v13
	v_mul_f32_e32 v24, v24, v24
	v_mul_f32_e32 v25, v25, v25
;     __device__ __forceinline__ void operator()(const f32x4 (&acc)[2][2][4][2], const Unit& u, int wr, int wc, int fr, int fq) const {
;         const int row0 = u.pm * BM + wr * 64 + fr, col0 = u.pn * BM + wc * 32 + 8 * fq;
; #pragma unroll
;         for (int ai = 0; ai < 2; ++ai)
; #pragma unroll
;             for (int m = 0; m < 4; ++m) {
;                 const int row = row0 + ai * HALF + m * 16;
;                 const float rs = rsqrtf(ss[row] * (1.0f / 4096.0f) + RMS_EPS) * (1.0f / 64.0f);
;                 unsigned char* rowp = U + ((size_t)(row >> 4) * 512 + (col0 >> 5)) * 512 + (row & 15) * 32 + (col0 & 31);
; #pragma unroll
;                 for (int bj = 0; bj < 2; ++bj) {
;                     f32x4 v0 = acc[ai][bj][m][0] * rs, v1 = acc[ai][bj][m][1] * rs;
; #pragma unroll
;                     for (int j = 0; j < 4; ++j) { const float a = fmaxf(v0[j], 0.f), b = fmaxf(v1[j], 0.f); v0[j] = a * a * 4.f; v1[j] = b * b * 4.f; }
;                     u32x2 w; w.x = pk4_fp8(v0[0], v0[1], v0[2], v0[3]); w.y = pk4_fp8(v1[0], v1[1], v1[2], v1[3]);
;                     *(u32x2*)(rowp + bj * (HALF / 32) * 512) = w;
;                 }
	v_mul_f32_e32 v14, 4.0, v14
	v_mul_f32_e32 v18, 4.0, v18
	v_mul_f32_e32 v15, 4.0, v15
	v_mul_f32_e32 v19, 4.0, v19
	v_mul_f32_e32 v22, 4.0, v22
	v_mul_f32_e32 v23, 4.0, v23
	v_mul_f32_e32 v24, 4.0, v24
	v_mul_f32_e32 v25, 4.0, v25
	v_med3_f32 v14, v14, s44, v195
	v_med3_f32 v15, v15, s44, v195
	v_med3_f32 v18, v18, s44, v195
	v_med3_f32 v19, v19, s44, v195
	v_med3_f32 v22, v22, s44, v195
	v_med3_f32 v3, v23, s44, v195
	v_cvt_pk_fp8_f32 v6, v14, v15 op_sel:[0,0,1]
	v_cvt_pk_fp8_f32 v7, v18, v19 op_sel:[0,0,1]
	v_cvt_pk_fp8_f32 v8, v22, v3 op_sel:[0,0,1]
	v_med3_f32 v3, v24, s44, v195
	v_med3_f32 v12, v25, s44, v195
	v_cvt_pk_fp8_f32 v9, v3, v12 op_sel:[0,0,1]
	global_store_dwordx2 v[10:11], v[6:7], off
	global_store_dwordx2 v[10:11], v[8:9], off offset:2048
	v_add_u32_e32 v9, 0x90, v2
	v_ashrrev_i32_e32 v10, 4, v9
	v_mov_b32_e32 v6, 0
	v_mov_b32_e32 v7, 0
	v_mov_b32_e32 v8, 0
	v_ashrrev_i32_e32 v11, 31, v10
	v_lshlrev_b64 v[10:11], 18, v[10:11]
	v_lshl_add_u64 v[10:11], s[24:25], 0, v[10:11]
	v_lshl_add_u64 v[10:11], v[10:11], 0, s[20:21]
	v_lshl_add_u64 v[10:11], v[10:11], 0, v[172:173]
	v_lshl_add_u64 v[10:11], v[10:11], 0, v[170:171]
	v_fmamk_f32 v3, v239, 0x39800000, v194
	v_mul_f32_e32 v9, 0x4b800000, v3
	v_cmp_gt_f32_e32 vcc, s43, v3
	s_nop 1
	v_cndmask_b32_e32 v3, v3, v9, vcc
	v_rsq_f32_e32 v3, v3
	s_nop 0
	v_mul_f32_e32 v9, 0x45800000, v3
	v_cndmask_b32_e32 v3, v3, v9, vcc
	v_mul_f32_e32 v12, 0x3c800000, v3
	v_pk_mul_f32 v[16:17], v[78:79], v[12:13] op_sel_hi:[1,0]
	v_pk_mul_f32 v[20:21], v[74:75], v[12:13] op_sel_hi:[1,0]
	v_pk_mul_f32 v[14:15], v[80:81], v[12:13] op_sel_hi:[1,0]
	v_pk_mul_f32 v[18:19], v[76:77], v[12:13] op_sel_hi:[1,0]
	v_pk_mul_f32 v[22:23], v[72:73], v[12:13] op_sel_hi:[1,0]
	v_pk_mul_f32 v[24:25], v[70:71], v[12:13] op_sel_hi:[1,0]
	v_pk_mul_f32 v[26:27], v[68:69], v[12:13] op_sel_hi:[1,0]
	v_pk_mul_f32 v[12:13], v[66:67], v[12:13] op_sel_hi:[1,0]
	v_max_f32_e32 v3, 0, v16
	v_max_f32_e32 v9, 0, v20
	v_max_f32_e32 v16, 0, v17
	v_max_f32_e32 v17, 0, v21
	v_max_f32_e32 v20, 0, v24
	v_max_f32_e32 v12, 0, v12
	v_max_f32_e32 v21, 0, v25
	v_max_f32_e32 v13, 0, v13
	v_mul_f32_e32 v3, v3, v3
	v_mul_f32_e32 v9, v9, v9
	v_mul_f32_e32 v16, v16, v16
	v_mul_f32_e32 v17, v17, v17
	v_mul_f32_e32 v20, v20, v20
	v_mul_f32_e32 v12, v12, v12
	v_mul_f32_e32 v21, v21, v21
	v_mul_f32_e32 v13, v13, v13
	v_mul_f32_e32 v3, 4.0, v3
	v_mul_f32_e32 v9, 4.0, v9
	v_mul_f32_e32 v16, 4.0, v16
	v_mul_f32_e32 v17, 4.0, v17
	v_mul_f32_e32 v20, 4.0, v20
	v_mul_f32_e32 v12, 4.0, v12
	v_mul_f32_e32 v21, 4.0, v21
	v_mul_f32_e32 v13, 4.0, v13
	v_med3_f32 v3, v3, s44, v195
	v_med3_f32 v16, v16, s44, v195
	v_med3_f32 v9, v9, s44, v195
	v_med3_f32 v17, v17, s44, v195
	v_max_f32_e32 v14, 0, v14
	v_max_f32_e32 v18, 0, v18
	v_max_f32_e32 v15, 0, v15
	v_max_f32_e32 v19, 0, v19
	v_med3_f32 v20, v20, s44, v195
	v_med3_f32 v21, v21, s44, v195
	v_cvt_pk_fp8_f32 v6, v3, v16
	v_cvt_pk_fp8_f32 v7, v9, v17
	v_med3_f32 v3, v12, s44, v195
	v_med3_f32 v12, v13, s44, v195
	v_mov_b32_e32 v9, 0
	v_max_f32_e32 v22, 0, v22
	v_max_f32_e32 v24, 0, v26
	v_max_f32_e32 v23, 0, v23
	v_max_f32_e32 v25, 0, v27
	v_mul_f32_e32 v14, v14, v14
	v_mul_f32_e32 v18, v18, v18
	v_mul_f32_e32 v15, v15, v15
	v_mul_f32_e32 v19, v19, v19
	v_cvt_pk_fp8_f32 v8, v20, v21
	v_cvt_pk_fp8_f32 v9, v3, v12
	v_mul_f32_e32 v22, v22, v22
	v_mul_f32_e32 v24, v24, v24
	v_mul_f32_e32 v23, v23, v23
	v_mul_f32_e32 v25, v25, v25
	v_mul_f32_e32 v14, 4.0, v14
	v_mul_f32_e32 v18, 4.0, v18
	v_mul_f32_e32 v15, 4.0, v15
	v_mul_f32_e32 v19, 4.0, v19
	v_mul_f32_e32 v22, 4.0, v22
	v_mul_f32_e32 v24, 4.0, v24
	v_mul_f32_e32 v23, 4.0, v23
	v_mul_f32_e32 v25, 4.0, v25
	v_med3_f32 v14, v14, s44, v195
	v_med3_f32 v15, v15, s44, v195
	v_med3_f32 v18, v18, s44, v195
	v_med3_f32 v19, v19, s44, v195
	v_med3_f32 v22, v22, s44, v195
	v_med3_f32 v23, v23, s44, v195
	v_cvt_pk_fp8_f32 v6, v14, v15 op_sel:[0,0,1]
	v_cvt_pk_fp8_f32 v7, v18, v19 op_sel:[0,0,1]
	v_med3_f32 v3, v24, s44, v195
	v_med3_f32 v12, v25, s44, v195
	v_cvt_pk_fp8_f32 v8, v22, v23 op_sel:[0,0,1]
	v_cvt_pk_fp8_f32 v9, v3, v12 op_sel:[0,0,1]
	global_store_dwordx2 v[10:11], v[6:7], off
	global_store_dwordx2 v[10:11], v[8:9], off offset:2048
	v_add_u32_e32 v9, 0xa0, v2
	v_ashrrev_i32_e32 v10, 4, v9
	v_mov_b32_e32 v6, 0
	v_mov_b32_e32 v7, 0
	v_mov_b32_e32 v8, 0
	v_ashrrev_i32_e32 v11, 31, v10
	v_lshlrev_b64 v[10:11], 18, v[10:11]
	v_lshl_add_u64 v[10:11], s[24:25], 0, v[10:11]
	v_lshl_add_u64 v[10:11], v[10:11], 0, s[20:21]
	v_lshl_add_u64 v[10:11], v[10:11], 0, v[172:173]
	v_lshl_add_u64 v[10:11], v[10:11], 0, v[170:171]
	v_add_u32_e32 v2, 0xb0, v2
	v_ashrrev_i32_e32 v2, 4, v2
	v_fmamk_f32 v3, v240, 0x39800000, v194
	v_mul_f32_e32 v9, 0x4b800000, v3
	v_cmp_gt_f32_e32 vcc, s43, v3
	s_nop 1
	v_cndmask_b32_e32 v3, v3, v9, vcc
	v_rsq_f32_e32 v3, v3
	s_nop 0
	v_mul_f32_e32 v9, 0x45800000, v3
	v_cndmask_b32_e32 v3, v3, v9, vcc
	v_mul_f32_e32 v12, 0x3c800000, v3
	v_pk_mul_f32 v[16:17], v[62:63], v[12:13] op_sel_hi:[1,0]
	v_pk_mul_f32 v[20:21], v[58:59], v[12:13] op_sel_hi:[1,0]
	v_pk_mul_f32 v[14:15], v[64:65], v[12:13] op_sel_hi:[1,0]
	v_pk_mul_f32 v[18:19], v[60:61], v[12:13] op_sel_hi:[1,0]
	v_pk_mul_f32 v[22:23], v[56:57], v[12:13] op_sel_hi:[1,0]
	v_pk_mul_f32 v[24:25], v[54:55], v[12:13] op_sel_hi:[1,0]
	v_pk_mul_f32 v[26:27], v[52:53], v[12:13] op_sel_hi:[1,0]
	v_pk_mul_f32 v[12:13], v[50:51], v[12:13] op_sel_hi:[1,0]
	v_max_f32_e32 v3, 0, v16
	v_max_f32_e32 v9, 0, v20
	v_max_f32_e32 v16, 0, v17
	v_max_f32_e32 v17, 0, v21
	v_max_f32_e32 v20, 0, v24
	v_max_f32_e32 v12, 0, v12
	v_max_f32_e32 v21, 0, v25
;     __device__ __forceinline__ void operator()(const f32x4 (&acc)[2][2][4][2], const Unit& u, int wr, int wc, int fr, int fq) const {
;         const int row0 = u.pm * BM + wr * 64 + fr, col0 = u.pn * BM + wc * 32 + 8 * fq;
; #pragma unroll
;         for (int ai = 0; ai < 2; ++ai)
; #pragma unroll
;             for (int m = 0; m < 4; ++m) {
;                 const int row = row0 + ai * HALF + m * 16;
;                 const float rs = rsqrtf(ss[row] * (1.0f / 4096.0f) + RMS_EPS) * (1.0f / 64.0f);
;                 unsigned char* rowp = U + ((size_t)(row >> 4) * 512 + (col0 >> 5)) * 512 + (row & 15) * 32 + (col0 & 31);
; #pragma unroll
;                 for (int bj = 0; bj < 2; ++bj) {
;                     f32x4 v0 = acc[ai][bj][m][0] * rs, v1 = acc[ai][bj][m][1] * rs;
; #pragma unroll
;                     for (int j = 0; j < 4; ++j) { const float a = fmaxf(v0[j], 0.f), b = fmaxf(v1[j], 0.f); v0[j] = a * a * 4.f; v1[j] = b * b * 4.f; }
;                     u32x2 w; w.x = pk4_fp8(v0[0], v0[1], v0[2], v0[3]); w.y = pk4_fp8(v1[0], v1[1], v1[2], v1[3]);
;                     *(u32x2*)(rowp + bj * (HALF / 32) * 512) = w;
;                 }
	v_max_f32_e32 v13, 0, v13
	v_mul_f32_e32 v3, v3, v3
	v_mul_f32_e32 v9, v9, v9
	v_mul_f32_e32 v16, v16, v16
	v_mul_f32_e32 v17, v17, v17
	v_mul_f32_e32 v20, v20, v20
	v_mul_f32_e32 v12, v12, v12
	v_mul_f32_e32 v21, v21, v21
	v_mul_f32_e32 v13, v13, v13
	v_mul_f32_e32 v3, 4.0, v3
	v_mul_f32_e32 v9, 4.0, v9
	v_mul_f32_e32 v16, 4.0, v16
	v_mul_f32_e32 v17, 4.0, v17
	v_mul_f32_e32 v20, 4.0, v20
	v_mul_f32_e32 v12, 4.0, v12
	v_mul_f32_e32 v21, 4.0, v21
	v_mul_f32_e32 v13, 4.0, v13
	v_med3_f32 v3, v3, s44, v195
	v_med3_f32 v16, v16, s44, v195
	v_med3_f32 v9, v9, s44, v195
	v_med3_f32 v17, v17, s44, v195
	v_max_f32_e32 v14, 0, v14
	v_max_f32_e32 v18, 0, v18
	v_max_f32_e32 v15, 0, v15
	v_max_f32_e32 v19, 0, v19
	v_med3_f32 v20, v20, s44, v195
	v_med3_f32 v21, v21, s44, v195
	v_med3_f32 v12, v12, s44, v195
	v_cvt_pk_fp8_f32 v6, v3, v16
	v_cvt_pk_fp8_f32 v7, v9, v17
	v_med3_f32 v3, v13, s44, v195
	v_mov_b32_e32 v9, 0
	v_max_f32_e32 v22, 0, v22
	v_max_f32_e32 v24, 0, v26
	v_max_f32_e32 v23, 0, v23
	v_max_f32_e32 v25, 0, v27
	v_mul_f32_e32 v14, v14, v14
	v_mul_f32_e32 v18, v18, v18
	v_mul_f32_e32 v15, v15, v15
	v_mul_f32_e32 v19, v19, v19
	v_cvt_pk_fp8_f32 v8, v20, v21
	v_cvt_pk_fp8_f32 v9, v12, v3
	v_mul_f32_e32 v22, v22, v22
	v_mul_f32_e32 v24, v24, v24
	v_mul_f32_e32 v23, v23, v23
	v_mul_f32_e32 v25, v25, v25
	v_mul_f32_e32 v14, 4.0, v14
	v_mul_f32_e32 v18, 4.0, v18
	v_mul_f32_e32 v15, 4.0, v15
	v_mul_f32_e32 v19, 4.0, v19
	v_mul_f32_e32 v22, 4.0, v22
	v_mul_f32_e32 v24, 4.0, v24
	v_mul_f32_e32 v23, 4.0, v23
	v_mul_f32_e32 v25, 4.0, v25
	v_med3_f32 v14, v14, s44, v195
	v_med3_f32 v15, v15, s44, v195
	v_med3_f32 v18, v18, s44, v195
	v_med3_f32 v19, v19, s44, v195
	v_med3_f32 v22, v22, s44, v195
	v_med3_f32 v23, v23, s44, v195
	v_cvt_pk_fp8_f32 v6, v14, v15 op_sel:[0,0,1]
	v_cvt_pk_fp8_f32 v7, v18, v19 op_sel:[0,0,1]
	v_med3_f32 v3, v24, s44, v195
	v_med3_f32 v12, v25, s44, v195
	v_cvt_pk_fp8_f32 v8, v22, v23 op_sel:[0,0,1]
	v_cvt_pk_fp8_f32 v9, v3, v12 op_sel:[0,0,1]
	global_store_dwordx2 v[10:11], v[6:7], off
	global_store_dwordx2 v[10:11], v[8:9], off offset:2048
	v_mov_b32_e32 v4, 0
	v_mov_b32_e32 v5, 0
	v_mov_b32_e32 v6, 0
	v_mov_b32_e32 v7, 0
	v_ashrrev_i32_e32 v3, 31, v2
	v_lshlrev_b64 v[2:3], 18, v[2:3]
	v_lshl_add_u64 v[2:3], s[24:25], 0, v[2:3]
	v_lshl_add_u64 v[2:3], v[2:3], 0, s[20:21]
	v_lshl_add_u64 v[2:3], v[2:3], 0, v[172:173]
	v_lshl_add_u64 v[2:3], v[2:3], 0, v[170:171]
	v_fmamk_f32 v8, v241, 0x39800000, v194
	v_mul_f32_e32 v9, 0x4b800000, v8
	v_cmp_gt_f32_e32 vcc, s43, v8
	s_nop 1
	v_cndmask_b32_e32 v8, v8, v9, vcc
	v_rsq_f32_e32 v8, v8
	s_nop 0
	v_mul_f32_e32 v9, 0x45800000, v8
	v_cndmask_b32_e32 v8, v8, v9, vcc
	v_mul_f32_e32 v8, 0x3c800000, v8
	v_pk_mul_f32 v[12:13], v[46:47], v[8:9] op_sel_hi:[1,0]
	v_pk_mul_f32 v[16:17], v[42:43], v[8:9] op_sel_hi:[1,0]
	v_pk_mul_f32 v[10:11], v[48:49], v[8:9] op_sel_hi:[1,0]
	v_pk_mul_f32 v[14:15], v[44:45], v[8:9] op_sel_hi:[1,0]
	v_pk_mul_f32 v[18:19], v[40:41], v[8:9] op_sel_hi:[1,0]
	v_pk_mul_f32 v[20:21], v[38:39], v[8:9] op_sel_hi:[1,0]
	v_pk_mul_f32 v[22:23], v[36:37], v[8:9] op_sel_hi:[1,0]
	v_pk_mul_f32 v[8:9], v[34:35], v[8:9] op_sel_hi:[1,0]
	v_max_f32_e32 v12, 0, v12
	v_max_f32_e32 v16, 0, v16
	v_max_f32_e32 v13, 0, v13
	v_max_f32_e32 v17, 0, v17
	v_max_f32_e32 v20, 0, v20
	v_max_f32_e32 v8, 0, v8
	v_max_f32_e32 v21, 0, v21
	v_max_f32_e32 v9, 0, v9
	v_mul_f32_e32 v12, v12, v12
	v_mul_f32_e32 v16, v16, v16
	v_mul_f32_e32 v13, v13, v13
	v_mul_f32_e32 v17, v17, v17
	v_mul_f32_e32 v20, v20, v20
	v_mul_f32_e32 v8, v8, v8
	v_mul_f32_e32 v21, v21, v21
	v_mul_f32_e32 v9, v9, v9
	v_mul_f32_e32 v12, 4.0, v12
	v_mul_f32_e32 v16, 4.0, v16
	v_mul_f32_e32 v13, 4.0, v13
	v_mul_f32_e32 v17, 4.0, v17
	v_mul_f32_e32 v20, 4.0, v20
	v_mul_f32_e32 v8, 4.0, v8
	v_mul_f32_e32 v21, 4.0, v21
	v_mul_f32_e32 v9, 4.0, v9
	v_med3_f32 v12, v12, s44, v195
	v_med3_f32 v13, v13, s44, v195
	v_med3_f32 v16, v16, s44, v195
	v_med3_f32 v17, v17, s44, v195
	v_max_f32_e32 v10, 0, v10
	v_max_f32_e32 v14, 0, v14
	v_max_f32_e32 v11, 0, v11
	v_max_f32_e32 v15, 0, v15
	v_med3_f32 v20, v20, s44, v195
	v_med3_f32 v21, v21, s44, v195
	v_med3_f32 v8, v8, s44, v195
	v_cvt_pk_fp8_f32 v4, v12, v13
	v_cvt_pk_fp8_f32 v5, v16, v17
	v_med3_f32 v9, v9, s44, v195
	v_max_f32_e32 v18, 0, v18
	v_max_f32_e32 v22, 0, v22
	v_max_f32_e32 v19, 0, v19
	v_max_f32_e32 v23, 0, v23
	v_mul_f32_e32 v10, v10, v10
	v_mul_f32_e32 v14, v14, v14
	v_mul_f32_e32 v11, v11, v11
	v_mul_f32_e32 v15, v15, v15
	v_cvt_pk_fp8_f32 v6, v20, v21
	v_cvt_pk_fp8_f32 v7, v8, v9
	v_mul_f32_e32 v18, v18, v18
	v_mul_f32_e32 v22, v22, v22
	v_mul_f32_e32 v19, v19, v19
	v_mul_f32_e32 v23, v23, v23
	v_mul_f32_e32 v10, 4.0, v10
	v_mul_f32_e32 v14, 4.0, v14
	v_mul_f32_e32 v11, 4.0, v11
	v_mul_f32_e32 v15, 4.0, v15
	v_mul_f32_e32 v18, 4.0, v18
	v_mul_f32_e32 v22, 4.0, v22
	v_mul_f32_e32 v19, 4.0, v19
	v_mul_f32_e32 v23, 4.0, v23
	v_med3_f32 v10, v10, s44, v195
	v_med3_f32 v11, v11, s44, v195
	v_med3_f32 v14, v14, s44, v195
	v_med3_f32 v15, v15, s44, v195
	v_med3_f32 v18, v18, s44, v195
	v_med3_f32 v19, v19, s44, v195
	v_cvt_pk_fp8_f32 v4, v10, v11 op_sel:[0,0,1]
	v_cvt_pk_fp8_f32 v5, v14, v15 op_sel:[0,0,1]
	v_med3_f32 v8, v22, s44, v195
	v_med3_f32 v9, v23, s44, v195
	v_cvt_pk_fp8_f32 v6, v18, v19 op_sel:[0,0,1]
	v_cvt_pk_fp8_f32 v7, v8, v9 op_sel:[0,0,1]
	s_andn2_b64 vcc, exec, s[0:1]
	s_mov_b64 s[0:1], -1
	global_store_dwordx2 v[2:3], v[4:5], off
	global_store_dwordx2 v[2:3], v[6:7], off offset:2048
	s_cbranch_vccnz .LBB0_2273
	s_andn2_b64 vcc, exec, s[4:5]
	s_cbranch_vccnz .LBB0_2272
	s_barrier
	s_branch .LBB0_2272

; __global__ void __launch_bounds__(NWAVES * 64, 2) mk_fwd(Args args) {
	.amdhsa_kernel _Z6mk_fwd4Args
		.amdhsa_group_segment_fixed_size 0
		.amdhsa_private_segment_fixed_size 0
		.amdhsa_kernarg_size 440
		.amdhsa_user_sgpr_count 2
		.amdhsa_user_sgpr_dispatch_ptr 0
		.amdhsa_user_sgpr_queue_ptr 0
		.amdhsa_user_sgpr_kernarg_segment_ptr 1
		.amdhsa_user_sgpr_dispatch_id 0
		.amdhsa_user_sgpr_kernarg_preload_length 0
		.amdhsa_user_sgpr_kernarg_preload_offset 0
		.amdhsa_user_sgpr_private_segment_size 0
		.amdhsa_uses_dynamic_stack 0
		.amdhsa_enable_private_segment 0
		.amdhsa_system_sgpr_workgroup_id_x 1
		.amdhsa_system_sgpr_workgroup_id_y 0
		.amdhsa_system_sgpr_workgroup_id_z 0
		.amdhsa_system_sgpr_workgroup_info 0
		.amdhsa_system_vgpr_workitem_id 0
		.amdhsa_next_free_vgpr 254
		.amdhsa_next_free_sgpr 102
		.amdhsa_accum_offset 256
		.amdhsa_reserve_vcc 1
		.amdhsa_float_round_mode_32 0
		.amdhsa_float_round_mode_16_64 0
		.amdhsa_float_denorm_mode_32 3
		.amdhsa_float_denorm_mode_16_64 3
		.amdhsa_dx10_clamp 1
		.amdhsa_ieee_mode 1
		.amdhsa_fp16_overflow 0
		.amdhsa_tg_split 0
		.amdhsa_exception_fp_ieee_invalid_op 0
		.amdhsa_exception_fp_denorm_src 0
		.amdhsa_exception_fp_ieee_div_zero 0
		.amdhsa_exception_fp_ieee_overflow 0
		.amdhsa_exception_fp_ieee_underflow 0
		.amdhsa_exception_fp_ieee_inexact 0
		.amdhsa_exception_int_div_zero 0
	.end_amdhsa_kernel

; __global__ void __launch_bounds__(NWAVES * 64, 2) mk_fwd(Args args) {
amdhsa.kernels:
  - .agpr_count:     0
    .args:
      - .offset:         0
        .size:           184
        .value_kind:     by_value
      - .offset:         184
        .size:           4
        .value_kind:     hidden_block_count_x
      - .offset:         188
        .size:           4
        .value_kind:     hidden_block_count_y
      - .offset:         192
        .size:           4
        .value_kind:     hidden_block_count_z
      - .offset:         196
        .size:           2
        .value_kind:     hidden_group_size_x
      - .offset:         198
        .size:           2
        .value_kind:     hidden_group_size_y
      - .offset:         200
        .size:           2
        .value_kind:     hidden_group_size_z
      - .offset:         202
        .size:           2
        .value_kind:     hidden_remainder_x
      - .offset:         204
        .size:           2
        .value_kind:     hidden_remainder_y
      - .offset:         206
        .size:           2
        .value_kind:     hidden_remainder_z
      - .offset:         224
        .size:           8
        .value_kind:     hidden_global_offset_x
      - .offset:         232
        .size:           8
        .value_kind:     hidden_global_offset_y
      - .offset:         240
        .size:           8
        .value_kind:     hidden_global_offset_z
      - .offset:         248
        .size:           2
        .value_kind:     hidden_grid_dims
      - .offset:         304
        .size:           4
        .value_kind:     hidden_dynamic_lds_size
    .group_segment_fixed_size: 0
    .kernarg_segment_align: 8
    .kernarg_segment_size: 440
    .language:       OpenCL C
    .language_version:
      - 2
      - 0
    .max_flat_workgroup_size: 512
    .name:           _Z6mk_fwd4Args
    .private_segment_fixed_size: 0
    .sgpr_count:     108
    .sgpr_spill_count: 117
    .symbol:         _Z6mk_fwd4Args.kd
    .uniform_work_group_size: 1
    .uses_dynamic_stack: false
    .vgpr_count:     254
    .vgpr_spill_count: 0
    .wavefront_size: 64
